# combo17 + strategy 7: 98 dead zero-inits (v_mov_b32 vN, v185 before a v_cvt_pk_fp8_f32 low/high pair) removed from the fp8 epilogues (48 deleted, 50 kept as s_nop 0 where a producer/consumer pair cros
# baseline (speedup 1.0000x reference)
.LBB0_151:
	v_lshl_add_u64 v[10:11], s[6:7], 0, v[2:3]
	s_brev_b32 s2, 34
	s_ashr_i32 s5, s4, 11
	v_add_co_u32_e64 v10, s[2:3], s2, v10
	s_add_i32 s9, s21, s5
	s_nop 0
	v_addc_co_u32_e64 v11, s[2:3], 0, v11, s[2:3]
	s_mul_hi_i32 s3, s9, 0x6000
	s_mulk_i32 s9, 0x6000
	s_add_u32 s2, s0, s9
	v_lshl_add_u64 v[14:15], s[6:7], 0, v[6:7]
	s_addc_u32 s3, s1, s3
	v_add_co_u32_e32 v14, vcc, 0x34000000, v14
	v_lshl_add_u64 v[32:33], s[2:3], 0, v[184:185]
	s_mov_b64 s[2:3], 0x5000
	v_addc_co_u32_e32 v15, vcc, 0, v15, vcc
	s_add_i32 s5, s5, s20
	v_lshl_add_u64 v[54:55], v[32:33], 0, s[2:3]
	s_movk_i32 s2, 0x5000
	s_mul_hi_i32 s9, s5, 0x6000
	s_mulk_i32 s5, 0x6000
	v_add_co_u32_e32 v32, vcc, s2, v32
	v_lshl_add_u64 v[8:9], s[6:7], 0, v[4:5]
	s_add_u32 s16, s0, s5
	s_mov_b64 s[2:3], vcc
	s_brev_b32 s5, 61
	v_add_co_u32_e32 v56, vcc, s5, v8
	v_addc_co_u32_e64 v33, s[2:3], 0, v33, s[2:3]
	s_mov_b32 s5, 0xbc001000
	s_mov_b64 s[2:3], vcc
	v_add_co_u32_e32 v58, vcc, s5, v8
	v_addc_co_u32_e64 v57, s[2:3], 0, v9, s[2:3]
	s_nop 0
	v_addc_co_u32_e32 v59, vcc, 0, v9, vcc
	global_load_dwordx4 v[20:23], v[14:15], off
	global_load_dwordx4 v[24:27], v[14:15], off offset:1024
	global_load_dwordx4 v[28:31], v[14:15], off offset:2048
	global_load_dwordx4 v[42:45], v[14:15], off offset:3072
	global_load_dwordx4 v[46:49], v[54:55], off offset:16
	global_load_dwordx4 v[50:53], v[32:33], off
	global_load_dwordx2 v[60:61], v[56:57], off offset:1024
	global_load_dwordx2 v[62:63], v[56:57], off offset:2048
	global_load_dwordx2 v[64:65], v[56:57], off offset:3072
	global_load_dwordx2 v[66:67], v[58:59], off offset:-4096
	s_addc_u32 s17, s1, s9
	s_add_u32 s18, s16, 0x1000
	s_addc_u32 s19, s17, 0
	v_mov_b32_e32 v37, 0x43e00000
	v_mov_b32_e32 v38, 0x43e00000
	v_mov_b32_e32 v16, v185
	v_mov_b32_e32 v17, v185
	v_mov_b32_e32 v39, 0x43e00000
	v_mov_b32_e32 v40, 0x43e00000
	v_mov_b32_e32 v18, v185
	v_mov_b32_e32 v19, v185
	v_mov_b32_e32 v35, 0x43e00000
	v_mov_b32_e32 v36, 0x43e00000
	v_mov_b32_e32 v12, v185
	v_mov_b32_e32 v13, v185
	s_add_i32 s4, s4, s8
	v_lshl_add_u64 v[2:3], v[2:3], 0, s[10:11]
	v_lshl_add_u64 v[4:5], v[4:5], 0, s[12:13]
	v_lshl_add_u64 v[6:7], v[6:7], 0, s[14:15]
	s_cmp_lt_i32 s4, 0x10000
	s_waitcnt vmcnt(0)
	v_lshlrev_b32_e32 v78, 16, v24
	v_lshlrev_b32_e32 v68, 16, v20
	v_and_b32_e32 v69, 0xffff0000, v20
	v_lshlrev_b32_e32 v70, 16, v21
	v_and_b32_e32 v71, 0xffff0000, v21
	v_and_b32_e32 v79, 0xffff0000, v24
	v_lshlrev_b32_e32 v80, 16, v25
	v_cvt_pk_f32_fp8_e32 v[98:99], v66
	v_cvt_pk_f32_fp8_sdwa v[100:101], v66 src0_sel:WORD_1
	v_cvt_pk_f32_fp8_e32 v[102:103], v67
	v_cvt_pk_f32_fp8_sdwa v[66:67], v67 src0_sel:WORD_1
	v_and_b32_e32 v81, 0xffff0000, v25
	v_lshlrev_b32_e32 v82, 16, v26
	v_and_b32_e32 v83, 0xffff0000, v26
	v_lshlrev_b32_e32 v84, 16, v27
	v_and_b32_e32 v85, 0xffff0000, v27
	v_lshlrev_b32_e32 v8, 16, v42
	v_and_b32_e32 v9, 0xffff0000, v42
	v_lshlrev_b32_e32 v20, 16, v43
	v_and_b32_e32 v21, 0xffff0000, v43
	v_lshlrev_b32_e32 v26, 16, v44
	v_and_b32_e32 v27, 0xffff0000, v44
	v_lshlrev_b32_e32 v32, 16, v45
	v_and_b32_e32 v33, 0xffff0000, v45
	v_cvt_pk_f32_fp8_e32 v[24:25], v60
	v_cvt_pk_f32_fp8_sdwa v[42:43], v60 src0_sel:WORD_1
	v_cvt_pk_f32_fp8_e32 v[44:45], v61
	v_cvt_pk_f32_fp8_sdwa v[60:61], v61 src0_sel:WORD_1
	v_cvt_pk_f32_fp8_e32 v[86:87], v62
	v_cvt_pk_f32_fp8_sdwa v[88:89], v62 src0_sel:WORD_1
	v_cvt_pk_f32_fp8_e32 v[90:91], v63
	v_cvt_pk_f32_fp8_sdwa v[62:63], v63 src0_sel:WORD_1
	v_cvt_pk_f32_fp8_e32 v[92:93], v64
	v_cvt_pk_f32_fp8_sdwa v[94:95], v64 src0_sel:WORD_1
	v_cvt_pk_f32_fp8_e32 v[96:97], v65
	v_cvt_pk_f32_fp8_sdwa v[64:65], v65 src0_sel:WORD_1
	v_pk_add_f32 v[98:99], v[98:99], 0 op_sel_hi:[1,0]
	v_pk_add_f32 v[100:101], v[100:101], 0 op_sel_hi:[1,0]
	v_pk_add_f32 v[102:103], v[102:103], 0 op_sel_hi:[1,0]
	v_pk_add_f32 v[66:67], v[66:67], 0 op_sel_hi:[1,0]
	v_pk_add_f32 v[24:25], v[98:99], v[24:25]
	v_pk_add_f32 v[42:43], v[100:101], v[42:43]
	v_pk_add_f32 v[44:45], v[102:103], v[44:45]
	v_pk_add_f32 v[60:61], v[66:67], v[60:61]
	v_pk_add_f32 v[24:25], v[24:25], v[86:87]
	v_pk_add_f32 v[42:43], v[42:43], v[88:89]
	v_pk_add_f32 v[44:45], v[44:45], v[90:91]
	v_pk_add_f32 v[60:61], v[60:61], v[62:63]
	v_pk_add_f32 v[24:25], v[24:25], v[92:93]
	v_pk_add_f32 v[42:43], v[42:43], v[94:95]
	v_pk_add_f32 v[44:45], v[44:45], v[96:97]
	v_pk_add_f32 v[60:61], v[60:61], v[64:65]
	v_lshlrev_b32_e32 v72, 16, v22
	v_and_b32_e32 v73, 0xffff0000, v22
	v_lshlrev_b32_e32 v22, 16, v23
	v_and_b32_e32 v23, 0xffff0000, v23
	v_pk_mul_f32 v[24:25], v[24:25], s[66:67] op_sel_hi:[1,0]
	v_pk_mul_f32 v[42:43], v[42:43], s[66:67] op_sel_hi:[1,0]
	v_pk_mul_f32 v[44:45], v[44:45], s[66:67] op_sel_hi:[1,0]
	v_pk_mul_f32 v[60:61], v[60:61], s[66:67] op_sel_hi:[1,0]
	v_pk_fma_f32 v[24:25], v[50:51], v[24:25], v[68:69]
	v_pk_fma_f32 v[42:43], v[52:53], v[42:43], v[70:71]
	v_pk_fma_f32 v[44:45], v[46:47], v[44:45], v[72:73]
	v_pk_fma_f32 v[60:61], v[48:49], v[60:61], v[22:23]
	v_cvt_pk_bf16_f32 v22, v24, v25
	v_cvt_pk_bf16_f32 v23, v42, v43
	v_cvt_pk_bf16_f32 v24, v44, v45
	v_cvt_pk_bf16_f32 v25, v60, v61
	global_store_dwordx4 v[14:15], v[22:25], off
	v_lshlrev_b32_e32 v41, 16, v22
	v_and_b32_e32 v100, 0xffff0000, v22
	v_lshlrev_b32_e32 v101, 16, v23
	v_and_b32_e32 v102, 0xffff0000, v23
	v_lshlrev_b32_e32 v61, 16, v25
	v_lshlrev_b32_e32 v60, 16, v24
	v_and_b32_e32 v63, 0xffff0000, v25
	v_and_b32_e32 v62, 0xffff0000, v24
	global_load_dwordx2 v[22:23], v[58:59], off
	global_load_dwordx2 v[24:25], v[58:59], off offset:1024
	global_load_dwordx2 v[42:43], v[58:59], off offset:2048
	global_load_dwordx2 v[44:45], v[58:59], off offset:3072
	v_mul_f32_e32 v66, v100, v100
	v_mul_f32_e32 v67, v102, v102
	v_pk_mul_f32 v[64:65], v[62:63], v[62:63]
	v_fmac_f32_e32 v66, v41, v41
	v_fmac_f32_e32 v67, v101, v101
	v_pk_fma_f32 v[64:65], v[60:61], v[60:61], v[64:65]
	v_add_f32_e32 v66, v66, v67
	v_add_f32_e32 v64, v66, v64
	v_add_f32_e32 v103, v64, v65
	v_lshlrev_b32_e32 v74, 16, v28
	v_and_b32_e32 v75, 0xffff0000, v28
	v_lshlrev_b32_e32 v28, 16, v29
	v_and_b32_e32 v29, 0xffff0000, v29
	v_lshlrev_b32_e32 v76, 16, v30
	v_and_b32_e32 v77, 0xffff0000, v30
	v_lshlrev_b32_e32 v30, 16, v31
	v_and_b32_e32 v31, 0xffff0000, v31
	s_waitcnt vmcnt(3)
	v_cvt_pk_f32_fp8_e32 v[64:65], v22
	v_cvt_pk_f32_fp8_sdwa v[66:67], v22 src0_sel:WORD_1
	v_cvt_pk_f32_fp8_e32 v[68:69], v23
	v_cvt_pk_f32_fp8_sdwa v[22:23], v23 src0_sel:WORD_1
	s_waitcnt vmcnt(2)
	v_cvt_pk_f32_fp8_e32 v[70:71], v24
	v_cvt_pk_f32_fp8_sdwa v[72:73], v24 src0_sel:WORD_1
	v_cvt_pk_f32_fp8_e32 v[86:87], v25
	v_cvt_pk_f32_fp8_sdwa v[24:25], v25 src0_sel:WORD_1
	s_waitcnt vmcnt(1)
	v_cvt_pk_f32_fp8_e32 v[88:89], v42
	v_cvt_pk_f32_fp8_sdwa v[90:91], v42 src0_sel:WORD_1
	v_cvt_pk_f32_fp8_e32 v[92:93], v43
	v_cvt_pk_f32_fp8_sdwa v[42:43], v43 src0_sel:WORD_1
	s_waitcnt vmcnt(0)
	v_cvt_pk_f32_fp8_e32 v[94:95], v44
	v_cvt_pk_f32_fp8_sdwa v[96:97], v44 src0_sel:WORD_1
	v_cvt_pk_f32_fp8_e32 v[98:99], v45
	v_cvt_pk_f32_fp8_sdwa v[44:45], v45 src0_sel:WORD_1
	v_pk_add_f32 v[64:65], v[64:65], 0 op_sel_hi:[1,0]
	v_pk_add_f32 v[66:67], v[66:67], 0 op_sel_hi:[1,0]
	v_pk_add_f32 v[68:69], v[68:69], 0 op_sel_hi:[1,0]
	v_pk_add_f32 v[22:23], v[22:23], 0 op_sel_hi:[1,0]
	v_pk_add_f32 v[64:65], v[64:65], v[70:71]
	v_pk_add_f32 v[66:67], v[66:67], v[72:73]
	v_pk_add_f32 v[68:69], v[68:69], v[86:87]
	v_pk_add_f32 v[22:23], v[22:23], v[24:25]
	v_pk_add_f32 v[24:25], v[64:65], v[88:89]
	v_pk_add_f32 v[64:65], v[66:67], v[90:91]
	v_pk_add_f32 v[66:67], v[68:69], v[92:93]
	v_pk_add_f32 v[22:23], v[22:23], v[42:43]
	v_pk_add_f32 v[24:25], v[24:25], v[94:95]
	v_pk_add_f32 v[42:43], v[64:65], v[96:97]
	v_pk_add_f32 v[64:65], v[66:67], v[98:99]
	v_pk_add_f32 v[22:23], v[22:23], v[44:45]
	v_pk_mul_f32 v[24:25], v[24:25], s[66:67] op_sel_hi:[1,0]
	v_pk_mul_f32 v[42:43], v[42:43], s[66:67] op_sel_hi:[1,0]
	v_pk_mul_f32 v[44:45], v[64:65], s[66:67] op_sel_hi:[1,0]
	v_pk_mul_f32 v[22:23], v[22:23], s[66:67] op_sel_hi:[1,0]
	v_pk_fma_f32 v[24:25], v[50:51], v[24:25], v[74:75]
	v_pk_fma_f32 v[28:29], v[52:53], v[42:43], v[28:29]
	v_pk_fma_f32 v[42:43], v[46:47], v[44:45], v[76:77]
	v_pk_fma_f32 v[30:31], v[48:49], v[22:23], v[30:31]
	v_cvt_pk_bf16_f32 v22, v24, v25
	v_cvt_pk_bf16_f32 v23, v28, v29
	v_cvt_pk_bf16_f32 v24, v42, v43
	v_cvt_pk_bf16_f32 v25, v30, v31
	global_store_dwordx4 v[14:15], v[22:25], off offset:2048
	v_lshlrev_b32_e32 v92, 16, v22
	v_and_b32_e32 v93, 0xffff0000, v22
	v_lshlrev_b32_e32 v94, 16, v23
	v_and_b32_e32 v95, 0xffff0000, v23
	v_lshlrev_b32_e32 v67, 16, v25
	v_lshlrev_b32_e32 v66, 16, v24
	v_and_b32_e32 v69, 0xffff0000, v25
	v_and_b32_e32 v68, 0xffff0000, v24
	global_load_dwordx2 v[22:23], v[56:57], off offset:512
	global_load_dwordx2 v[24:25], v[56:57], off offset:1536
	global_load_dwordx2 v[28:29], v[56:57], off offset:2560
	global_load_dwordx2 v[30:31], v[56:57], off offset:3584
	global_load_dwordx4 v[42:45], v[54:55], off offset:2048
	global_load_dwordx4 v[46:49], v[54:55], off offset:2064
	v_mul_f32_e32 v52, v93, v93
	v_mul_f32_e32 v53, v95, v95
	v_pk_mul_f32 v[50:51], v[68:69], v[68:69]
	v_fmac_f32_e32 v52, v92, v92
	v_fmac_f32_e32 v53, v94, v94
	v_pk_fma_f32 v[50:51], v[66:67], v[66:67], v[50:51]
	v_add_f32_e32 v52, v52, v53
	v_add_f32_e32 v50, v52, v50
	v_add_f32_e32 v96, v50, v51
	s_waitcnt vmcnt(5)
	v_cvt_pk_f32_fp8_e32 v[50:51], v22
	v_cvt_pk_f32_fp8_sdwa v[52:53], v22 src0_sel:WORD_1
	v_cvt_pk_f32_fp8_e32 v[54:55], v23
	v_cvt_pk_f32_fp8_sdwa v[22:23], v23 src0_sel:WORD_1
	s_waitcnt vmcnt(4)
	v_cvt_pk_f32_fp8_e32 v[56:57], v24
	v_cvt_pk_f32_fp8_sdwa v[64:65], v24 src0_sel:WORD_1
	v_cvt_pk_f32_fp8_e32 v[70:71], v25
	v_cvt_pk_f32_fp8_sdwa v[24:25], v25 src0_sel:WORD_1
	s_waitcnt vmcnt(3)
	v_cvt_pk_f32_fp8_e32 v[72:73], v28
	v_cvt_pk_f32_fp8_sdwa v[74:75], v28 src0_sel:WORD_1
	v_cvt_pk_f32_fp8_e32 v[76:77], v29
	v_cvt_pk_f32_fp8_sdwa v[28:29], v29 src0_sel:WORD_1
	s_waitcnt vmcnt(2)
	v_cvt_pk_f32_fp8_e32 v[86:87], v30
	v_cvt_pk_f32_fp8_sdwa v[88:89], v30 src0_sel:WORD_1
	v_cvt_pk_f32_fp8_e32 v[90:91], v31
	v_cvt_pk_f32_fp8_sdwa v[30:31], v31 src0_sel:WORD_1
	v_pk_add_f32 v[50:51], v[50:51], 0 op_sel_hi:[1,0]
	v_pk_add_f32 v[52:53], v[52:53], 0 op_sel_hi:[1,0]
	v_pk_add_f32 v[54:55], v[54:55], 0 op_sel_hi:[1,0]
	v_pk_add_f32 v[22:23], v[22:23], 0 op_sel_hi:[1,0]
	v_pk_add_f32 v[50:51], v[50:51], v[56:57]
	v_pk_add_f32 v[52:53], v[52:53], v[64:65]
	v_pk_add_f32 v[54:55], v[54:55], v[70:71]
	v_pk_add_f32 v[22:23], v[22:23], v[24:25]
	v_pk_add_f32 v[24:25], v[50:51], v[72:73]
	v_pk_add_f32 v[50:51], v[52:53], v[74:75]
	v_pk_add_f32 v[52:53], v[54:55], v[76:77]
	v_pk_add_f32 v[22:23], v[22:23], v[28:29]
	v_pk_add_f32 v[24:25], v[24:25], v[86:87]
	v_pk_add_f32 v[28:29], v[50:51], v[88:89]
	v_pk_add_f32 v[50:51], v[52:53], v[90:91]
	v_pk_add_f32 v[22:23], v[22:23], v[30:31]
	v_pk_mul_f32 v[24:25], v[24:25], s[66:67] op_sel_hi:[1,0]
	v_pk_mul_f32 v[28:29], v[28:29], s[66:67] op_sel_hi:[1,0]
	v_pk_mul_f32 v[30:31], v[50:51], s[66:67] op_sel_hi:[1,0]
	v_pk_mul_f32 v[22:23], v[22:23], s[66:67] op_sel_hi:[1,0]
	s_waitcnt vmcnt(1)
	v_pk_fma_f32 v[24:25], v[42:43], v[24:25], v[78:79]
	v_pk_fma_f32 v[50:51], v[44:45], v[28:29], v[80:81]
	s_waitcnt vmcnt(0)
	v_pk_fma_f32 v[30:31], v[46:47], v[30:31], v[82:83]
	v_pk_fma_f32 v[22:23], v[48:49], v[22:23], v[84:85]
	v_cvt_pk_bf16_f32 v28, v24, v25
	v_cvt_pk_bf16_f32 v29, v50, v51
	v_cvt_pk_bf16_f32 v30, v30, v31
	v_cvt_pk_bf16_f32 v31, v22, v23
	global_store_dwordx4 v[14:15], v[28:31], off offset:1024
	global_load_dwordx2 v[50:51], v[58:59], off offset:512
	global_load_dwordx2 v[52:53], v[58:59], off offset:1536
	global_load_dwordx2 v[54:55], v[58:59], off offset:2560
	global_load_dwordx2 v[56:57], v[58:59], off offset:3584
	v_lshlrev_b32_e32 v25, 16, v29
	v_lshlrev_b32_e32 v24, 16, v28
	v_and_b32_e32 v29, 0xffff0000, v29
	v_and_b32_e32 v28, 0xffff0000, v28
	v_pk_mul_f32 v[58:59], v[28:29], v[28:29]
	v_lshlrev_b32_e32 v23, 16, v31
	v_lshlrev_b32_e32 v22, 16, v30
	v_and_b32_e32 v31, 0xffff0000, v31
	v_and_b32_e32 v30, 0xffff0000, v30
	v_pk_fma_f32 v[58:59], v[24:25], v[24:25], v[58:59]
	v_pk_mul_f32 v[64:65], v[30:31], v[30:31]
	v_add_f32_e32 v58, v103, v58
	v_pk_fma_f32 v[64:65], v[22:23], v[22:23], v[64:65]
	v_add_f32_e32 v58, v58, v59
	v_add_f32_e32 v58, v58, v64
	v_add_f32_e32 v58, v58, v65
	s_waitcnt vmcnt(2)
	v_cvt_pk_f32_fp8_e32 v[64:65], v52
	v_add_f32_dpp v58, v58, v58 row_shr:1 row_mask:0xf bank_mask:0xf bound_ctrl:1
	v_cvt_pk_f32_fp8_sdwa v[70:71], v52 src0_sel:WORD_1
	v_cvt_pk_f32_fp8_e32 v[72:73], v53
	v_add_f32_dpp v58, v58, v58 row_shr:2 row_mask:0xf bank_mask:0xf bound_ctrl:1
	v_cvt_pk_f32_fp8_sdwa v[52:53], v53 src0_sel:WORD_1
	s_waitcnt vmcnt(1)
	v_cvt_pk_f32_fp8_e32 v[74:75], v54
	v_add_f32_dpp v58, v58, v58 row_shr:4 row_mask:0xf bank_mask:0xf bound_ctrl:1
	v_cvt_pk_f32_fp8_sdwa v[76:77], v54 src0_sel:WORD_1
	v_cvt_pk_f32_fp8_e32 v[78:79], v55
	v_add_f32_dpp v58, v58, v58 row_shr:8 row_mask:0xf bank_mask:0xf bound_ctrl:1
	v_cvt_pk_f32_fp8_sdwa v[54:55], v55 src0_sel:WORD_1
	v_readlane_b32 s5, v58, 31
	v_readlane_b32 s9, v58, 63
	v_readlane_b32 s2, v58, 15
	v_readlane_b32 s3, v58, 47
	v_mov_b32_e32 v58, s5
	v_mov_b32_e32 v59, s9
	v_pk_add_f32 v[58:59], s[2:3], v[58:59]
	s_waitcnt vmcnt(0)
	v_cvt_pk_f32_fp8_e32 v[80:81], v56
	v_add_f32_e32 v58, v58, v59
	v_fmamk_f32 v58, v58, 0x3a800000, v252
	v_rsq_f32_e32 v86, v58
	v_cvt_pk_f32_fp8_e32 v[58:59], v50
	v_cvt_pk_f32_fp8_sdwa v[82:83], v56 src0_sel:WORD_1
	v_cvt_pk_f32_fp8_e32 v[84:85], v57
	v_mul_f32_e32 v90, v86, v60
	v_mul_f32_e32 v91, v86, v62
	v_mul_f32_e32 v97, v86, v61
	v_mul_f32_e32 v98, v86, v63
	v_cvt_pk_f32_fp8_sdwa v[60:61], v50 src0_sel:WORD_1
	v_cvt_pk_f32_fp8_e32 v[62:63], v51
	v_cvt_pk_f32_fp8_sdwa v[50:51], v51 src0_sel:WORD_1
	v_cvt_pk_f32_fp8_sdwa v[56:57], v57 src0_sel:WORD_1
	v_pk_add_f32 v[58:59], v[58:59], 0 op_sel_hi:[1,0]
	v_pk_add_f32 v[60:61], v[60:61], 0 op_sel_hi:[1,0]
	v_pk_add_f32 v[62:63], v[62:63], 0 op_sel_hi:[1,0]
	v_pk_add_f32 v[50:51], v[50:51], 0 op_sel_hi:[1,0]
	v_pk_add_f32 v[58:59], v[58:59], v[64:65]
	v_pk_add_f32 v[60:61], v[60:61], v[70:71]
	v_pk_add_f32 v[62:63], v[62:63], v[72:73]
	v_pk_add_f32 v[50:51], v[50:51], v[52:53]
	v_pk_add_f32 v[52:53], v[58:59], v[74:75]
	v_pk_add_f32 v[58:59], v[60:61], v[76:77]
	v_pk_add_f32 v[60:61], v[62:63], v[78:79]
	v_pk_add_f32 v[50:51], v[50:51], v[54:55]
	v_pk_add_f32 v[52:53], v[52:53], v[80:81]
	v_pk_add_f32 v[54:55], v[58:59], v[82:83]
	v_pk_add_f32 v[58:59], v[60:61], v[84:85]
	v_pk_add_f32 v[50:51], v[50:51], v[56:57]
	v_pk_mul_f32 v[52:53], v[52:53], s[66:67] op_sel_hi:[1,0]
	v_pk_mul_f32 v[54:55], v[54:55], s[66:67] op_sel_hi:[1,0]
	v_pk_mul_f32 v[56:57], v[58:59], s[66:67] op_sel_hi:[1,0]
	v_pk_mul_f32 v[50:51], v[50:51], s[66:67] op_sel_hi:[1,0]
	v_pk_fma_f32 v[8:9], v[42:43], v[52:53], v[8:9]
	v_pk_fma_f32 v[20:21], v[44:45], v[54:55], v[20:21]
	v_pk_fma_f32 v[26:27], v[46:47], v[56:57], v[26:27]
	v_pk_fma_f32 v[32:33], v[48:49], v[50:51], v[32:33]
	v_cvt_pk_bf16_f32 v42, v8, v9
	v_cvt_pk_bf16_f32 v43, v20, v21
	v_cvt_pk_bf16_f32 v44, v26, v27
	v_cvt_pk_bf16_f32 v45, v32, v33
	global_store_dwordx4 v[14:15], v[42:45], off offset:3072
	v_lshlrev_b32_e32 v9, 16, v43
	v_lshlrev_b32_e32 v8, 16, v42
	v_and_b32_e32 v27, 0xffff0000, v43
	v_and_b32_e32 v26, 0xffff0000, v42
	v_lshlrev_b32_e32 v33, 16, v45
	v_lshlrev_b32_e32 v32, 16, v44
	v_and_b32_e32 v71, 0xffff0000, v45
	v_and_b32_e32 v70, 0xffff0000, v44
	global_load_dwordx4 v[42:45], v184, s[18:19]
	global_load_dwordx4 v[46:49], v184, s[18:19] offset:16
	global_load_dwordx4 v[50:53], v[0:1], off
	global_load_dwordx4 v[54:57], v[0:1], off offset:16
	global_load_dwordx4 v[58:61], v184, s[16:17]
	global_load_dwordx4 v[62:65], v184, s[16:17] offset:16
	v_pk_mul_f32 v[14:15], v[26:27], v[26:27]
	v_pk_mul_f32 v[20:21], v[70:71], v[70:71]
	v_pk_fma_f32 v[14:15], v[8:9], v[8:9], v[14:15]
	v_pk_fma_f32 v[20:21], v[32:33], v[32:33], v[20:21]
	v_add_f32_e32 v14, v96, v14
	v_add_f32_e32 v14, v14, v15
	v_add_f32_e32 v14, v14, v20
	v_add_f32_e32 v14, v14, v21
	v_mul_f32_e32 v41, v86, v41
	v_mul_f32_e32 v87, v86, v100
	v_add_f32_dpp v14, v14, v14 row_shr:1 row_mask:0xf bank_mask:0xf bound_ctrl:1
	v_mul_f32_e32 v88, v86, v101
	v_mul_f32_e32 v89, v86, v102
	v_add_f32_dpp v14, v14, v14 row_shr:2 row_mask:0xf bank_mask:0xf bound_ctrl:1
	v_mul_f32_e32 v24, v86, v24
	v_mul_f32_e32 v28, v86, v28
	v_add_f32_dpp v14, v14, v14 row_shr:4 row_mask:0xf bank_mask:0xf bound_ctrl:1
	v_mul_f32_e32 v22, v86, v22
	v_mul_f32_e32 v30, v86, v30
	v_add_f32_dpp v14, v14, v14 row_shr:8 row_mask:0xf bank_mask:0xf bound_ctrl:1
	v_mul_f32_e32 v25, v86, v25
	v_readlane_b32 s5, v14, 31
	v_readlane_b32 s9, v14, 63
	v_readlane_b32 s2, v14, 15
	v_readlane_b32 s3, v14, 47
	v_mov_b32_e32 v14, s5
	v_mov_b32_e32 v15, s9
	v_pk_add_f32 v[14:15], s[2:3], v[14:15]
	v_mul_f32_e32 v29, v86, v29
	v_add_f32_e32 v14, v14, v15
	v_fmamk_f32 v14, v14, 0x3a800000, v252
	v_rsq_f32_e32 v72, v14
	v_mul_f32_e32 v23, v86, v23
	v_mul_f32_e32 v31, v86, v31
	v_mul_f32_e32 v14, v72, v92
	v_mul_f32_e32 v15, v72, v93
	v_mul_f32_e32 v20, v72, v94
	v_mul_f32_e32 v21, v72, v95
	v_mul_f32_e32 v66, v72, v66
	v_mul_f32_e32 v68, v72, v68
	v_mul_f32_e32 v69, v72, v69
	v_mul_f32_e32 v67, v72, v67
	v_mul_f32_e32 v8, v72, v8
	v_mul_f32_e32 v26, v72, v26
	v_mul_f32_e32 v9, v72, v9
	v_mul_f32_e32 v32, v72, v32
	v_mul_f32_e32 v27, v72, v27
	v_mul_f32_e32 v33, v72, v33
	s_waitcnt vmcnt(5)
	v_add_f32_e32 v42, 1.0, v42
	s_waitcnt vmcnt(4)
	v_add_f32_e32 v46, 1.0, v46
	v_add_f32_e32 v43, 1.0, v43
	v_add_f32_e32 v47, 1.0, v47
	s_waitcnt vmcnt(3)
	v_mul_f32_e32 v41, v41, v50
	v_mul_f32_e32 v73, v87, v51
	s_waitcnt vmcnt(2)
	v_mul_f32_e32 v76, v90, v54
	v_mul_f32_e32 v77, v91, v55
	v_add_f32_e32 v44, 1.0, v44
	v_add_f32_e32 v45, 1.0, v45
	v_mul_f32_e32 v74, v88, v52
	v_mul_f32_e32 v75, v89, v53
	v_mul_f32_e32 v79, v98, v57
	v_mul_f32_e32 v14, v50, v14
	v_mul_f32_e32 v15, v51, v15
	v_mul_f32_e32 v20, v52, v20
	v_mul_f32_e32 v21, v53, v21
	v_mul_f32_e32 v50, v54, v66
	v_mul_f32_e32 v51, v55, v68
	v_mul_f32_e32 v53, v57, v69
	s_waitcnt vmcnt(1)
	v_fma_f32 v41, v41, v42, v58
	v_fma_f32 v54, v73, v43, v59
	s_waitcnt vmcnt(0)
	v_fma_f32 v57, v76, v46, v62
	v_fma_f32 v66, v77, v47, v63
	v_mul_f32_e32 v78, v97, v56
	v_mul_f32_e32 v52, v56, v67
	v_fma_f32 v55, v74, v44, v60
	v_fma_f32 v56, v75, v45, v61
	v_fma_f32 v14, v42, v14, v58
	v_fma_f32 v20, v44, v20, v60
	v_fmac_f32_e32 v61, v45, v21
	v_fma_f32 v21, v50, v46, v62
	v_fma_f32 v42, v51, v47, v63
	v_med3_f32 v41, v41, -v37, v37
	v_med3_f32 v44, v54, -v37, v37
	v_med3_f32 v46, v57, -v38, v38
	v_med3_f32 v47, v66, -v38, v38
	v_cvt_pk_fp8_f32 v16, v41, v44
	v_cvt_pk_fp8_f32 v17, v46, v47
	v_add_f32_e32 v48, 1.0, v48
	v_add_f32_e32 v49, 1.0, v49
	v_fma_f32 v67, v78, v48, v64
	v_fma_f32 v68, v79, v49, v65
	v_fma_f32 v15, v43, v15, v59
	v_fma_f32 v43, v52, v48, v64
	v_med3_f32 v45, v55, -v37, v37
	v_med3_f32 v37, v56, -v37, v37
	v_med3_f32 v48, v67, -v38, v38
	v_med3_f32 v38, v68, -v38, v38
	v_cvt_pk_fp8_f32 v16, v45, v37 op_sel:[0,0,1]
	v_cvt_pk_fp8_f32 v17, v48, v38 op_sel:[0,0,1]
	v_fmac_f32_e32 v65, v53, v49
	v_mul_f32_e32 v57, v72, v70
	v_mul_f32_e32 v58, v72, v71
	global_store_dwordx2 v[10:11], v[16:17], off
	v_mov_b32_e32 v56, 0x43e00000
	v_med3_f32 v14, v14, -v39, v39
	v_med3_f32 v15, v15, -v39, v39
	v_med3_f32 v16, v20, -v39, v39
	v_med3_f32 v20, v21, -v40, v40
	v_med3_f32 v21, v42, -v40, v40
	v_cvt_pk_fp8_f32 v18, v14, v15
	v_cvt_pk_fp8_f32 v19, v20, v21
	v_med3_f32 v17, v61, -v39, v39
	v_med3_f32 v37, v43, -v40, v40
	v_med3_f32 v38, v65, -v40, v40
	v_cvt_pk_fp8_f32 v18, v16, v17 op_sel:[0,0,1]
	v_cvt_pk_fp8_f32 v19, v37, v38 op_sel:[0,0,1]
	v_mov_b32_e32 v37, 0x43e00000
	s_nop 0
	s_nop 0
	global_store_dwordx2 v[10:11], v[18:19], off offset:1024
	global_load_dwordx4 v[14:17], v34, s[18:19]
	s_nop 0
	global_load_dwordx4 v[18:21], v34, s[18:19] offset:16
	global_load_dwordx4 v[38:41], v[0:1], off offset:2048
	global_load_dwordx4 v[42:45], v[0:1], off offset:2064
	global_load_dwordx4 v[46:49], v184, s[16:17] offset:2048
	global_load_dwordx4 v[50:53], v184, s[16:17] offset:2064
	s_waitcnt vmcnt(5)
	v_add_f32_e32 v14, 1.0, v14
	s_waitcnt vmcnt(4)
	v_add_f32_e32 v18, 1.0, v18
	v_add_f32_e32 v15, 1.0, v15
	v_add_f32_e32 v19, 1.0, v19
	s_waitcnt vmcnt(3)
	v_mul_f32_e32 v24, v24, v38
	v_mul_f32_e32 v28, v28, v39
	s_waitcnt vmcnt(2)
	v_mul_f32_e32 v22, v22, v42
	v_mul_f32_e32 v30, v30, v43
	v_add_f32_e32 v16, 1.0, v16
	v_mul_f32_e32 v25, v25, v40
	v_mul_f32_e32 v8, v8, v38
	v_mul_f32_e32 v26, v26, v39
	v_mul_f32_e32 v9, v9, v40
	v_mul_f32_e32 v32, v32, v42
	v_mul_f32_e32 v38, v57, v43
	s_waitcnt vmcnt(1)
	v_fma_f32 v24, v24, v14, v46
	v_fma_f32 v28, v28, v15, v47
	s_waitcnt vmcnt(0)
	v_fma_f32 v22, v22, v18, v50
	v_fma_f32 v30, v30, v19, v51
	v_fma_f32 v25, v25, v16, v48
	v_fma_f32 v8, v8, v14, v46
	v_fma_f32 v14, v26, v15, v47
	v_fma_f32 v9, v9, v16, v48
	v_fma_f32 v15, v32, v18, v50
	v_fma_f32 v16, v38, v19, v51
	v_med3_f32 v18, v24, -v35, v35
	v_med3_f32 v19, v28, -v35, v35
	v_med3_f32 v22, v22, -v36, v36
	v_med3_f32 v24, v30, -v36, v36
	v_cvt_pk_fp8_f32 v12, v18, v19
	v_cvt_pk_fp8_f32 v13, v22, v24
	v_add_f32_e32 v20, 1.0, v20
	v_add_f32_e32 v17, 1.0, v17
	v_add_f32_e32 v21, 1.0, v21
	v_mul_f32_e32 v29, v29, v41
	v_mul_f32_e32 v23, v23, v44
	v_mul_f32_e32 v31, v31, v45
	v_mul_f32_e32 v27, v27, v41
	v_mul_f32_e32 v33, v33, v44
	v_mul_f32_e32 v39, v58, v45
	v_fma_f32 v29, v29, v17, v49
	v_fma_f32 v23, v23, v20, v52
	v_fma_f32 v31, v31, v21, v53
	v_fmac_f32_e32 v49, v27, v17
	v_fma_f32 v17, v33, v20, v52
	v_fmac_f32_e32 v53, v39, v21
	v_med3_f32 v20, v25, -v35, v35
	v_med3_f32 v21, v29, -v35, v35
	v_med3_f32 v23, v23, -v36, v36
	v_med3_f32 v25, v31, -v36, v36
	v_cvt_pk_fp8_f32 v12, v20, v21 op_sel:[0,0,1]
	v_cvt_pk_fp8_f32 v13, v23, v25 op_sel:[0,0,1]
	global_store_dwordx2 v[10:11], v[12:13], off offset:512
	s_nop 0
	v_med3_f32 v8, v8, -v37, v37
	v_med3_f32 v12, v14, -v37, v37
	v_med3_f32 v14, v15, -v56, v56
	v_med3_f32 v15, v16, -v56, v56
	v_cvt_pk_fp8_f32 v54, v8, v12
	v_cvt_pk_fp8_f32 v55, v14, v15
	v_med3_f32 v9, v9, -v37, v37
	v_med3_f32 v13, v49, -v37, v37
	v_med3_f32 v8, v17, -v56, v56
	v_med3_f32 v12, v53, -v56, v56
	v_cvt_pk_fp8_f32 v54, v9, v13 op_sel:[0,0,1]
	v_cvt_pk_fp8_f32 v55, v8, v12 op_sel:[0,0,1]
	global_store_dwordx2 v[10:11], v[54:55], off offset:1536
	s_cbranch_scc1 .LBB0_151

.LBB0_156:
	s_movk_i32 s10, 0xe7f0
	global_load_dwordx4 v[0:3], v[36:37], off offset:-4096
	s_mov_b32 s11, -1
	global_load_dwordx4 v[16:19], v[36:37], off offset:-2064
	global_load_dwordx4 v[12:15], v[36:37], off offset:-2048
	v_lshl_add_u64 v[30:31], v[36:37], 0, s[10:11]
	v_add_co_u32_e32 v28, vcc, 0xfffff000, v36
	global_load_dwordx4 v[8:11], v[36:37], off offset:-16
	global_load_dwordx4 v[4:7], v[36:37], off
	s_ashr_i32 s3, s2, 11
	global_load_dwordx4 v[20:23], v[32:33], off offset:16
	global_load_dwordx4 v[24:27], v[32:33], off
	global_load_dwordx4 v[46:49], v[30:31], off offset:16
	s_mul_hi_i32 s5, s3, 0x6000
	s_mulk_i32 s3, 0x6000
	v_addc_co_u32_e32 v29, vcc, -1, v37, vcc
	global_load_dwordx4 v[50:53], v[28:29], off offset:-2064
	s_nop 0
	global_load_dwordx4 v[28:31], v[28:29], off offset:-16
	s_add_u32 s10, s0, s3
	s_addc_u32 s11, s1, s5
	s_add_u32 s12, s10, 0x1000
	s_addc_u32 s13, s11, 0
	global_load_dwordx4 v[54:57], v44, s[10:11] offset:16
	global_load_dwordx4 v[58:61], v44, s[10:11]
	global_load_dwordx4 v[62:65], v44, s[12:13]
	global_load_dwordx4 v[66:69], v44, s[12:13] offset:16
	v_mov_b32_e32 v90, 0x43e00000
	v_mov_b32_e32 v91, 0x43e00000
	v_mov_b32_e32 v92, 0x43e00000
	v_mov_b32_e32 v93, 0x43e00000
	v_mov_b32_e32 v94, 0x43e00000
	v_mov_b32_e32 v95, 0x43e00000
	v_mov_b32_e32 v96, 0x43e00000
	s_add_i32 s2, s2, s4
	v_lshl_add_u64 v[36:37], v[36:37], 0, s[8:9]
	s_cmp_gt_i32 s2, 0xffff
	s_waitcnt vmcnt(0)
	v_pk_mul_f32 v[70:71], v[2:3], v[2:3]
	v_pk_mul_f32 v[72:73], v[0:1], v[0:1]
	v_mul_f32_e32 v97, v17, v17
	v_mul_f32_e32 v98, v19, v19
	v_pk_mul_f32 v[74:75], v[14:15], v[14:15]
	v_pk_mul_f32 v[76:77], v[12:13], v[12:13]
	v_pk_mul_f32 v[78:79], v[10:11], v[10:11]
	v_pk_mul_f32 v[80:81], v[8:9], v[8:9]
	v_pk_mul_f32 v[82:83], v[6:7], v[6:7]
	v_pk_mul_f32 v[84:85], v[4:5], v[4:5]
	v_mov_b32_e32 v86, v70
	v_mov_b32_e32 v87, v72
	v_mov_b32_e32 v72, v71
	v_fmac_f32_e32 v97, v16, v16
	v_fmac_f32_e32 v98, v18, v18
	v_mov_b32_e32 v70, v74
	v_mov_b32_e32 v71, v76
	v_mov_b32_e32 v76, v75
	v_mov_b32_e32 v74, v78
	v_mov_b32_e32 v75, v80
	v_mov_b32_e32 v80, v79
	v_mov_b32_e32 v78, v82
	v_mov_b32_e32 v79, v84
	v_mov_b32_e32 v84, v83
	v_pk_mul_f32 v[82:83], v[48:49], v[48:49]
	v_pk_mul_f32 v[88:89], v[46:47], v[46:47]
	v_pk_add_f32 v[72:73], v[86:87], v[72:73]
	v_add_f32_e32 v86, v97, v98
	v_pk_add_f32 v[70:71], v[70:71], v[76:77]
	v_mul_f32_e32 v87, v51, v51
	v_mul_f32_e32 v97, v53, v53
	v_pk_add_f32 v[74:75], v[74:75], v[80:81]
	v_pk_add_f32 v[76:77], v[78:79], v[84:85]
	v_mov_b32_e32 v78, v82
	v_mov_b32_e32 v79, v88
	v_mov_b32_e32 v88, v83
	v_pk_mul_f32 v[80:81], v[30:31], v[30:31]
	v_pk_mul_f32 v[82:83], v[28:29], v[28:29]
	v_add_f32_e32 v71, v86, v71
	v_fmac_f32_e32 v87, v50, v50
	v_fmac_f32_e32 v97, v52, v52
	v_pk_add_f32 v[78:79], v[78:79], v[88:89]
	v_mov_b32_e32 v84, v80
	v_mov_b32_e32 v85, v82
	v_mov_b32_e32 v82, v81
	v_add_f32_e32 v80, v70, v71
	v_add_f32_e32 v81, v87, v97
	v_add_f32_e32 v75, v75, v80
	v_add_f32_e32 v79, v81, v79
	v_pk_add_f32 v[70:71], v[84:85], v[82:83]
	v_add_f32_e32 v74, v74, v75
	v_add_f32_e32 v75, 1.0, v62
	v_add_f32_e32 v62, v78, v79
	v_add_f32_e32 v80, 1.0, v63
	v_add_f32_e32 v63, v77, v74
	v_add_f32_e32 v62, v71, v62
	v_add_f32_e32 v63, v76, v63
	v_add_f32_e32 v62, v70, v62
	v_add_f32_e32 v62, v73, v62
	v_add_f32_dpp v63, v63, v63 row_shr:1 row_mask:0xf bank_mask:0xf bound_ctrl:1
	v_add_f32_e32 v62, v72, v62
	v_add_f32_e32 v66, 1.0, v66
	v_add_f32_dpp v63, v63, v63 row_shr:2 row_mask:0xf bank_mask:0xf bound_ctrl:1
	v_add_f32_dpp v62, v62, v62 row_shr:1 row_mask:0xf bank_mask:0xf bound_ctrl:1
	v_add_f32_e32 v67, 1.0, v67
	v_add_f32_dpp v63, v63, v63 row_shr:4 row_mask:0xf bank_mask:0xf bound_ctrl:1
	v_add_f32_dpp v62, v62, v62 row_shr:2 row_mask:0xf bank_mask:0xf bound_ctrl:1
	v_add_f32_e32 v65, 1.0, v65
	v_add_f32_dpp v63, v63, v63 row_shr:8 row_mask:0xf bank_mask:0xf bound_ctrl:1
	v_add_f32_dpp v70, v62, v62 row_shr:4 row_mask:0xf bank_mask:0xf bound_ctrl:1
	v_readlane_b32 s3, v63, 31
	v_readlane_b32 s5, v63, 63
	v_readlane_b32 s14, v63, 15
	v_readlane_b32 s15, v63, 47
	v_mov_b32_e32 v62, s3
	v_mov_b32_e32 v63, s5
	v_add_f32_dpp v70, v70, v70 row_shr:8 row_mask:0xf bank_mask:0xf bound_ctrl:1
	v_pk_add_f32 v[62:63], s[14:15], v[62:63]
	v_readlane_b32 s3, v70, 31
	v_readlane_b32 s5, v70, 63
	v_readlane_b32 s14, v70, 15
	v_readlane_b32 s15, v70, 47
	v_add_f32_e32 v70, v62, v63
	v_mov_b32_e32 v62, s3
	v_mov_b32_e32 v63, s5
	v_pk_add_f32 v[62:63], s[14:15], v[62:63]
	v_fmamk_f32 v70, v70, 0x3a800000, v252
	v_add_f32_e32 v62, v62, v63
	v_fmamk_f32 v62, v62, 0x3a800000, v252
	v_rsq_f32_e32 v70, v70
	v_rsq_f32_e32 v62, v62
	v_add_f32_e32 v69, 1.0, v69
	v_add_f32_e32 v64, 1.0, v64
	v_mul_f32_e32 v16, v16, v70
	v_mul_f32_e32 v17, v17, v70
	v_mul_f32_e32 v12, v12, v70
	v_mul_f32_e32 v13, v13, v70
	v_mul_f32_e32 v50, v50, v62
	v_mul_f32_e32 v51, v51, v62
	v_mul_f32_e32 v46, v46, v62
	v_mul_f32_e32 v47, v47, v62
	v_mul_f32_e32 v19, v19, v70
	v_mul_f32_e32 v15, v15, v70
	v_mul_f32_e32 v16, v24, v16
	v_mul_f32_e32 v17, v25, v17
	v_mul_f32_e32 v12, v20, v12
	v_mul_f32_e32 v13, v21, v13
	v_mul_f32_e32 v53, v53, v62
	v_mul_f32_e32 v49, v49, v62
	v_mul_f32_e32 v24, v50, v24
	v_mul_f32_e32 v25, v51, v25
	v_mul_f32_e32 v20, v46, v20
	v_mul_f32_e32 v21, v47, v21
	v_mul_f32_e32 v19, v27, v19
	v_mul_f32_e32 v15, v23, v15
	v_mul_f32_e32 v27, v53, v27
	v_mul_f32_e32 v23, v49, v23
	v_fma_f32 v24, v24, v75, v58
	v_fma_f32 v25, v25, v80, v59
	v_fma_f32 v20, v20, v66, v54
	v_fma_f32 v21, v21, v67, v55
	v_fma_f32 v27, v27, v65, v61
	v_fma_f32 v23, v23, v69, v57
	v_fmac_f32_e32 v61, v65, v19
	v_fmac_f32_e32 v57, v15, v69
	v_med3_f32 v15, v24, -v90, v90
	v_med3_f32 v19, v25, -v90, v90
	v_med3_f32 v20, v20, -v91, v91
	v_med3_f32 v21, v21, -v91, v91
	v_mul_f32_e32 v18, v18, v70
	v_mul_f32_e32 v14, v14, v70
	v_mul_f32_e32 v52, v52, v62
	v_mul_f32_e32 v48, v48, v62
	v_cvt_pk_fp8_f32 v40, v15, v19
	v_cvt_pk_fp8_f32 v41, v20, v21
	v_add_f32_e32 v68, 1.0, v68
	v_mul_f32_e32 v18, v26, v18
	v_mul_f32_e32 v14, v22, v14
	v_mul_f32_e32 v26, v52, v26
	v_mul_f32_e32 v22, v48, v22
	v_fma_f32 v26, v26, v64, v60
	v_fma_f32 v22, v22, v68, v56
	v_med3_f32 v24, v26, -v90, v90
	v_med3_f32 v25, v27, -v90, v90
	v_med3_f32 v22, v22, -v91, v91
	v_med3_f32 v23, v23, -v91, v91
	v_cvt_pk_fp8_f32 v40, v24, v25 op_sel:[0,0,1]
	v_cvt_pk_fp8_f32 v41, v22, v23 op_sel:[0,0,1]
	v_fma_f32 v16, v75, v16, v58
	v_fma_f32 v17, v80, v17, v59
	v_fma_f32 v12, v12, v66, v54
	v_fma_f32 v13, v13, v67, v55
	global_store_dwordx2 v[34:35], v[40:41], off offset:-1536
	v_fma_f32 v18, v64, v18, v60
	v_med3_f32 v15, v16, -v92, v92
	v_med3_f32 v16, v17, -v92, v92
	v_med3_f32 v12, v12, -v93, v93
	v_med3_f32 v13, v13, -v93, v93
	v_cvt_pk_fp8_f32 v42, v15, v16
	v_cvt_pk_fp8_f32 v43, v12, v13
	v_fma_f32 v14, v14, v68, v56
	v_med3_f32 v17, v18, -v92, v92
	v_med3_f32 v18, v61, -v92, v92
	v_med3_f32 v14, v14, -v93, v93
	v_med3_f32 v19, v57, -v93, v93
	v_cvt_pk_fp8_f32 v42, v17, v18 op_sel:[0,0,1]
	v_cvt_pk_fp8_f32 v43, v14, v19 op_sel:[0,0,1]
	v_mul_f32_e32 v28, v28, v62
	v_mul_f32_e32 v29, v29, v62
	v_mul_f32_e32 v0, v0, v62
	global_store_dwordx2 v[34:35], v[42:43], off offset:-512
	global_load_dwordx4 v[12:15], v45, s[12:13]
	global_load_dwordx4 v[16:19], v45, s[12:13] offset:16
	global_load_dwordx4 v[20:23], v[32:33], off offset:2048
	global_load_dwordx4 v[24:27], v[32:33], off offset:2064
	s_nop 0
	global_load_dwordx4 v[40:43], v44, s[10:11] offset:2048
	global_load_dwordx4 v[46:49], v44, s[10:11] offset:2064
	v_mul_f32_e32 v1, v1, v62
	v_mul_f32_e32 v8, v8, v70
	v_mul_f32_e32 v9, v9, v70
	v_mul_f32_e32 v11, v11, v70
	v_mul_f32_e32 v7, v7, v70
	v_mul_f32_e32 v31, v31, v62
	v_mul_f32_e32 v3, v3, v62
	v_mul_f32_e32 v30, v30, v62
	v_mul_f32_e32 v2, v2, v62
	v_mul_f32_e32 v10, v10, v70
	v_mul_f32_e32 v4, v4, v70
	v_mul_f32_e32 v5, v5, v70
	v_mov_b32_e32 v52, 0x43e00000
	v_mul_f32_e32 v6, v6, v70
	s_waitcnt vmcnt(5)
	v_add_f32_e32 v12, 1.0, v12
	s_waitcnt vmcnt(4)
	v_add_f32_e32 v16, 1.0, v16
	v_add_f32_e32 v13, 1.0, v13
	v_add_f32_e32 v17, 1.0, v17
	s_waitcnt vmcnt(3)
	v_mul_f32_e32 v28, v28, v20
	v_mul_f32_e32 v29, v29, v21
	s_waitcnt vmcnt(2)
	v_mul_f32_e32 v0, v0, v24
	v_mul_f32_e32 v1, v1, v25
	v_add_f32_e32 v15, 1.0, v15
	v_add_f32_e32 v19, 1.0, v19
	v_mul_f32_e32 v31, v31, v23
	v_mul_f32_e32 v3, v3, v27
	v_mul_f32_e32 v8, v8, v20
	v_mul_f32_e32 v9, v9, v21
	v_mul_f32_e32 v11, v11, v23
	v_mul_f32_e32 v7, v7, v27
	s_waitcnt vmcnt(1)
	v_fma_f32 v20, v28, v12, v40
	v_fma_f32 v21, v29, v13, v41
	s_waitcnt vmcnt(0)
	v_fma_f32 v0, v0, v16, v46
	v_fma_f32 v1, v1, v17, v47
	v_fma_f32 v23, v31, v15, v43
	v_fma_f32 v3, v3, v19, v49
	v_fmac_f32_e32 v43, v11, v15
	v_fmac_f32_e32 v49, v7, v19
	v_med3_f32 v7, v20, -v94, v94
	v_med3_f32 v11, v21, -v94, v94
	v_med3_f32 v0, v0, -v95, v95
	v_med3_f32 v1, v1, -v95, v95
	v_cvt_pk_fp8_f32 v38, v7, v11
	v_cvt_pk_fp8_f32 v39, v0, v1
	v_add_f32_e32 v14, 1.0, v14
	v_add_f32_e32 v18, 1.0, v18
	v_mul_f32_e32 v30, v30, v22
	v_mul_f32_e32 v2, v2, v26
	v_mul_f32_e32 v10, v10, v22
	v_fma_f32 v22, v30, v14, v42
	v_fma_f32 v2, v2, v18, v48
	v_fma_f32 v8, v8, v12, v40
	v_fma_f32 v9, v9, v13, v41
	v_med3_f32 v12, v22, -v94, v94
	v_med3_f32 v13, v23, -v94, v94
	v_med3_f32 v2, v2, -v95, v95
	v_med3_f32 v3, v3, -v95, v95
	v_cvt_pk_fp8_f32 v38, v12, v13 op_sel:[0,0,1]
	v_cvt_pk_fp8_f32 v39, v2, v3 op_sel:[0,0,1]
	v_mul_f32_e32 v4, v4, v24
	v_mul_f32_e32 v5, v5, v25
	v_fma_f32 v4, v4, v16, v46
	v_fma_f32 v5, v5, v17, v47
	global_store_dwordx2 v[34:35], v[38:39], off offset:-1024
	v_mul_f32_e32 v6, v6, v26
	v_med3_f32 v0, v8, -v96, v96
	v_med3_f32 v1, v9, -v96, v96
	v_med3_f32 v4, v4, -v52, v52
	v_med3_f32 v5, v5, -v52, v52
	v_cvt_pk_fp8_f32 v50, v0, v1
	v_cvt_pk_fp8_f32 v51, v4, v5
	v_fma_f32 v10, v10, v14, v42
	v_fma_f32 v6, v6, v18, v48
	v_med3_f32 v2, v10, -v96, v96
	v_med3_f32 v3, v43, -v96, v96
	v_med3_f32 v6, v6, -v52, v52
	v_med3_f32 v0, v49, -v52, v52
	v_cvt_pk_fp8_f32 v50, v2, v3 op_sel:[0,0,1]
	v_cvt_pk_fp8_f32 v51, v6, v0 op_sel:[0,0,1]
	global_store_dwordx2 v[34:35], v[50:51], off
	v_lshl_add_u64 v[34:35], v[34:35], 0, s[6:7]
	s_cbranch_scc0 .LBB0_156

.LBB0_526:
	v_or_b32_e32 v184, s5, v132
	v_lshl_add_u64 v[24:25], s[88:89], 0, v[184:185]
	v_lshlrev_b64 v[24:25], 10, v[24:25]
	v_lshl_add_u64 v[24:25], s[34:35], 0, v[24:25]
	v_lshlrev_b32_e32 v184, 4, v137
	v_lshl_add_u64 v[28:29], v[24:25], 0, v[184:185]
	v_rcp_f32_e32 v24, v96
	v_mov_b32_e32 v34, 0x43e00000
	s_ashr_i32 s4, s18, 1
	v_mul_f32_e32 v30, 0x41000000, v24
	v_pk_mul_f32 v[24:25], v[94:95], v[30:31] op_sel_hi:[1,0]
	v_pk_mul_f32 v[26:27], v[92:93], v[30:31] op_sel_hi:[1,0]
	v_med3_f32 v31, v24, -v34, v34
	v_med3_f32 v26, v26, -v34, v34
	v_med3_f32 v27, v27, -v34, v34
	s_nop 0
	v_cvt_pk_fp8_f32 v24, v26, v27
	v_med3_f32 v25, v25, -v34, v34
	v_pk_mul_f32 v[32:33], v[88:89], v[30:31] op_sel_hi:[1,0]
	v_pk_mul_f32 v[26:27], v[90:91], v[30:31] op_sel_hi:[1,0]
	v_cvt_pk_fp8_f32 v24, v31, v25 op_sel:[0,0,1]
	v_med3_f32 v31, v32, -v34, v34
	v_med3_f32 v32, v33, -v34, v34
	s_nop 0
	v_cvt_pk_fp8_f32 v25, v31, v32
	v_med3_f32 v26, v26, -v34, v34
	v_med3_f32 v27, v27, -v34, v34
	v_pk_mul_f32 v[32:33], v[76:77], v[30:31] op_sel_hi:[1,0]
	v_cvt_pk_fp8_f32 v25, v26, v27 op_sel:[0,0,1]
	v_pk_mul_f32 v[26:27], v[78:79], v[30:31] op_sel_hi:[1,0]
	v_med3_f32 v31, v32, -v34, v34
	v_med3_f32 v32, v33, -v34, v34
	v_med3_f32 v33, v26, -v34, v34
	s_nop 0
	v_cvt_pk_fp8_f32 v26, v31, v32
	v_med3_f32 v27, v27, -v34, v34
	s_and_b32 s4, s4, 0xffffff80
	s_ashr_i32 s5, s4, 31
	v_cvt_pk_fp8_f32 v26, v33, v27 op_sel:[0,0,1]
	v_pk_mul_f32 v[32:33], v[74:75], v[30:31] op_sel_hi:[1,0]
	v_pk_mul_f32 v[30:31], v[72:73], v[30:31] op_sel_hi:[1,0]
	s_nop 0
	v_med3_f32 v30, v30, -v34, v34
	v_med3_f32 v31, v31, -v34, v34
	v_cvt_pk_fp8_f32 v27, v30, v31
	v_med3_f32 v32, v32, -v34, v34
	v_med3_f32 v33, v33, -v34, v34
	v_lshl_add_u64 v[28:29], v[28:29], 0, s[4:5]
	s_mov_b64 s[4:5], 0x72000100
	v_cvt_pk_fp8_f32 v27, v32, v33 op_sel:[0,0,1]
	v_lshl_add_u64 v[30:31], v[28:29], 0, s[4:5]
	v_add_co_u32_e32 v28, vcc, s56, v28
	s_nop 1
	v_permlane16_swap_b32 v24, v25
	v_permlane16_swap_b32 v26, v27
	s_nop 1
	v_permlane32_swap_b32 v24, v26
	v_permlane32_swap_b32 v25, v27
	s_waitcnt vmcnt(2)
	v_mov_b64_e32 v[66:67], v[18:19]
	v_addc_co_u32_e32 v29, vcc, 0, v29, vcc
	global_store_dwordx4 v[28:29], v[24:27], off offset:256
	v_mov_b32_e32 v29, 0x43e00000
	v_mov_b64_e32 v[64:65], v[16:17]
	v_rcp_f32_e32 v24, v68
	s_waitcnt vmcnt(1)
	v_mov_b64_e32 v[70:71], v[22:23]
	v_mov_b64_e32 v[68:69], v[20:21]
	v_mul_f32_e32 v28, 0x41000000, v24
	v_pk_mul_f32 v[24:25], v[62:63], v[28:29] op_sel_hi:[1,0]
	v_pk_mul_f32 v[26:27], v[60:61], v[28:29] op_sel_hi:[1,0]
	v_med3_f32 v32, v24, -v29, v29
	v_med3_f32 v26, v26, -v29, v29
	v_med3_f32 v27, v27, -v29, v29
	s_nop 0
	v_cvt_pk_fp8_f32 v24, v26, v27
	v_med3_f32 v25, v25, -v29, v29
	v_pk_mul_f32 v[26:27], v[58:59], v[28:29] op_sel_hi:[1,0]
	v_pk_mul_f32 v[4:5], v[4:5], v[28:29] op_sel_hi:[1,0]
	v_cvt_pk_fp8_f32 v24, v32, v25 op_sel:[0,0,1]
	v_pk_mul_f32 v[32:33], v[56:57], v[28:29] op_sel_hi:[1,0]
	s_nop 0
	v_med3_f32 v32, v32, -v29, v29
	v_med3_f32 v33, v33, -v29, v29
	v_cvt_pk_fp8_f32 v25, v32, v33
	v_med3_f32 v26, v26, -v29, v29
	v_med3_f32 v27, v27, -v29, v29
	v_pk_mul_f32 v[0:1], v[0:1], v[28:29] op_sel_hi:[1,0]
	v_cvt_pk_fp8_f32 v25, v26, v27 op_sel:[0,0,1]
	v_med3_f32 v4, v4, -v29, v29
	v_med3_f32 v5, v5, -v29, v29
	v_med3_f32 v0, v0, -v29, v29
	v_med3_f32 v1, v1, -v29, v29
	s_nop 0
	v_cvt_pk_fp8_f32 v26, v4, v5
	v_cvt_pk_fp8_f32 v27, v0, v1
	v_pk_mul_f32 v[6:7], v[6:7], v[28:29] op_sel_hi:[1,0]
	v_pk_mul_f32 v[2:3], v[2:3], v[28:29] op_sel_hi:[1,0]
	v_med3_f32 v6, v6, -v29, v29
	v_med3_f32 v7, v7, -v29, v29
	v_med3_f32 v2, v2, -v29, v29
	v_med3_f32 v3, v3, -v29, v29
	v_mov_b64_e32 v[58:59], v[10:11]
	v_mov_b64_e32 v[62:63], v[14:15]
	v_cvt_pk_fp8_f32 v26, v6, v7 op_sel:[0,0,1]
	v_cvt_pk_fp8_f32 v27, v2, v3 op_sel:[0,0,1]
	v_mov_b64_e32 v[56:57], v[8:9]
	v_mov_b64_e32 v[60:61], v[12:13]
	s_nop 1
	v_permlane16_swap_b32 v24, v25
	v_permlane16_swap_b32 v26, v27
	s_nop 1
	v_permlane32_swap_b32 v24, v26
	v_permlane32_swap_b32 v25, v27
	global_store_dwordx4 v[30:31], v[24:27], off offset:64

.LBB0_602:
	v_rcp_f32_e32 v0, v108
	v_mov_b32_e32 v105, 0x43e00000
	v_lshlrev_b32_e32 v184, 4, v197
	v_mul_f32_e32 v4, 0x41000000, v0
	v_pk_mul_f32 v[0:1], v[100:101], v[4:5] op_sel_hi:[1,0]
	v_ashrrev_i32_e32 v197, 31, v196
	v_med3_f32 v2, v0, -v105, v105
	v_med3_f32 v1, v1, -v105, v105
	s_nop 0
	v_cvt_pk_fp8_f32 v0, v2, v1
	v_pk_mul_f32 v[2:3], v[102:103], v[4:5] op_sel_hi:[1,0]
	s_lshl_b32 s40, s74, 6
	v_med3_f32 v1, v2, -v105, v105
	v_med3_f32 v2, v3, -v105, v105
	v_cvt_pk_fp8_f32 v0, v1, v2 op_sel:[0,0,1]
	v_pk_mul_f32 v[2:3], v[96:97], v[4:5] op_sel_hi:[1,0]
	s_nop 0
	v_med3_f32 v2, v2, -v105, v105
	v_med3_f32 v3, v3, -v105, v105
	v_cvt_pk_fp8_f32 v1, v2, v3
	v_pk_mul_f32 v[2:3], v[98:99], v[4:5] op_sel_hi:[1,0]
	s_mov_b64 s[10:11], 0
	v_med3_f32 v2, v2, -v105, v105
	v_med3_f32 v3, v3, -v105, v105
	v_cvt_pk_fp8_f32 v1, v2, v3 op_sel:[0,0,1]
	v_pk_mul_f32 v[2:3], v[92:93], v[4:5] op_sel_hi:[1,0]
	s_nop 0
	v_med3_f32 v5, v2, -v105, v105
	v_med3_f32 v3, v3, -v105, v105
	s_nop 0
	v_cvt_pk_fp8_f32 v2, v5, v3
	v_pk_mul_f32 v[6:7], v[94:95], v[4:5] op_sel_hi:[1,0]
	s_nop 0
	v_med3_f32 v5, v7, -v105, v105
	v_med3_f32 v3, v6, -v105, v105
	v_pk_mul_f32 v[6:7], v[88:89], v[4:5] op_sel_hi:[1,0]
	v_cvt_pk_fp8_f32 v2, v3, v5 op_sel:[0,0,1]
	v_med3_f32 v5, v6, -v105, v105
	v_med3_f32 v6, v7, -v105, v105
	s_nop 0
	v_cvt_pk_fp8_f32 v3, v5, v6
	v_pk_mul_f32 v[4:5], v[90:91], v[4:5] op_sel_hi:[1,0]
	v_rcp_f32_e32 v6, v104
	v_med3_f32 v4, v4, -v105, v105
	v_med3_f32 v5, v5, -v105, v105
	v_cvt_pk_fp8_f32 v3, v4, v5 op_sel:[0,0,1]
	v_lshlrev_b64 v[4:5], 10, v[196:197]
	v_lshl_add_u64 v[4:5], s[86:87], 0, v[4:5]
	v_lshl_add_u64 v[4:5], v[4:5], 0, s[40:41]
	v_lshl_add_u64 v[4:5], v[4:5], 0, v[184:185]
	v_add_co_u32_e32 v4, vcc, s56, v4
	s_nop 1
	v_permlane16_swap_b32 v0, v1
	v_permlane16_swap_b32 v2, v3
	s_nop 1
	v_permlane32_swap_b32 v0, v2
	v_permlane32_swap_b32 v1, v3
	v_mov_b32_e32 v88, 0x43e00000
	s_nop 0
	v_addc_co_u32_e32 v5, vcc, 0, v5, vcc
	global_store_dwordx4 v[4:5], v[0:3], off offset:768
	v_mul_f32_e32 v4, 0x41000000, v6
	s_nop 0
	v_pk_mul_f32 v[0:1], v[84:85], v[4:5] op_sel_hi:[1,0]
	s_nop 0
	v_med3_f32 v2, v0, -v88, v88
	v_med3_f32 v1, v1, -v88, v88
	s_nop 0
	v_cvt_pk_fp8_f32 v0, v2, v1
	v_pk_mul_f32 v[2:3], v[86:87], v[4:5] op_sel_hi:[1,0]
	s_nop 0
	v_med3_f32 v1, v2, -v88, v88
	v_med3_f32 v2, v3, -v88, v88
	v_cvt_pk_fp8_f32 v0, v1, v2 op_sel:[0,0,1]
	v_pk_mul_f32 v[2:3], v[80:81], v[4:5] op_sel_hi:[1,0]
	s_nop 0
	v_med3_f32 v2, v2, -v88, v88
	v_med3_f32 v3, v3, -v88, v88
	v_cvt_pk_fp8_f32 v1, v2, v3
	v_pk_mul_f32 v[2:3], v[82:83], v[4:5] op_sel_hi:[1,0]
	s_nop 0
	v_med3_f32 v2, v2, -v88, v88
	v_med3_f32 v3, v3, -v88, v88
	v_cvt_pk_fp8_f32 v1, v2, v3 op_sel:[0,0,1]
	v_pk_mul_f32 v[2:3], v[76:77], v[4:5] op_sel_hi:[1,0]
	s_nop 0
	v_med3_f32 v5, v2, -v88, v88
	v_med3_f32 v3, v3, -v88, v88
	s_nop 0
	v_cvt_pk_fp8_f32 v2, v5, v3
	v_pk_mul_f32 v[6:7], v[78:79], v[4:5] op_sel_hi:[1,0]
	s_nop 0
	v_med3_f32 v5, v7, -v88, v88
	v_med3_f32 v3, v6, -v88, v88
	v_pk_mul_f32 v[6:7], v[72:73], v[4:5] op_sel_hi:[1,0]
	v_cvt_pk_fp8_f32 v2, v3, v5 op_sel:[0,0,1]
	v_med3_f32 v5, v6, -v88, v88
	v_med3_f32 v6, v7, -v88, v88
	s_nop 0
	v_cvt_pk_fp8_f32 v3, v5, v6
	v_pk_mul_f32 v[4:5], v[74:75], v[4:5] op_sel_hi:[1,0]
	s_nop 0
	v_med3_f32 v4, v4, -v88, v88
	v_med3_f32 v5, v5, -v88, v88
	v_cvt_pk_fp8_f32 v3, v4, v5 op_sel:[0,0,1]
	v_or_b32_e32 v4, 16, v196
	v_ashrrev_i32_e32 v5, 31, v4
	v_lshlrev_b64 v[4:5], 10, v[4:5]
	v_lshl_add_u64 v[4:5], s[86:87], 0, v[4:5]
	v_lshl_add_u64 v[4:5], v[4:5], 0, s[40:41]
	v_lshl_add_u64 v[4:5], v[4:5], 0, v[184:185]
	v_add_co_u32_e32 v4, vcc, 0x72000000, v4
	s_nop 1
	v_permlane16_swap_b32 v0, v1
	v_permlane16_swap_b32 v2, v3
	s_nop 1
	v_permlane32_swap_b32 v0, v2
	v_permlane32_swap_b32 v1, v3
	s_nop 1
	v_addc_co_u32_e32 v5, vcc, 0, v5, vcc
	global_store_dwordx4 v[4:5], v[0:3], off offset:768

.LBB0_623:
	s_waitcnt vmcnt(0)
	v_mov_b32_e32 v96, 0x43e00000
	v_pk_mul_f32 v[92:93], v[92:93], s[60:61] op_sel_hi:[1,0]
	v_pk_mul_f32 v[94:95], v[94:95], s[60:61] op_sel_hi:[1,0]
	v_med3_f32 v97, v92, -v96, v96
	v_med3_f32 v93, v93, -v96, v96
	s_nop 0
	v_cvt_pk_fp8_f32 v92, v97, v93
	v_med3_f32 v94, v94, -v96, v96
	v_med3_f32 v95, v95, -v96, v96
	v_pk_mul_f32 v[80:81], v[80:81], s[60:61] op_sel_hi:[1,0]
	v_cvt_pk_fp8_f32 v92, v94, v95 op_sel:[0,0,1]
	v_pk_mul_f32 v[88:89], v[88:89], s[60:61] op_sel_hi:[1,0]
	v_pk_mul_f32 v[84:85], v[84:85], s[60:61] op_sel_hi:[1,0]
	v_med3_f32 v80, v80, -v96, v96
	v_med3_f32 v81, v81, -v96, v96
	v_ashrrev_i32_e32 v125, 31, v124
	v_med3_f32 v88, v88, -v96, v96
	v_med3_f32 v89, v89, -v96, v96
	v_med3_f32 v84, v84, -v96, v96
	v_med3_f32 v85, v85, -v96, v96
	v_cvt_pk_fp8_f32 v95, v80, v81
	v_lshlrev_b64 v[80:81], 10, v[124:125]
	s_lshl_b32 s40, s74, 6
	v_cvt_pk_fp8_f32 v93, v88, v89
	v_cvt_pk_fp8_f32 v94, v84, v85
	v_lshl_add_u64 v[80:81], s[86:87], 0, v[80:81]
	v_mov_b32_e32 v121, v185
	v_lshl_add_u64 v[80:81], v[80:81], 0, s[40:41]
	v_pk_mul_f32 v[90:91], v[90:91], s[60:61] op_sel_hi:[1,0]
	v_pk_mul_f32 v[86:87], v[86:87], s[60:61] op_sel_hi:[1,0]
	v_pk_mul_f32 v[82:83], v[82:83], s[60:61] op_sel_hi:[1,0]
	v_lshl_add_u64 v[80:81], v[80:81], 0, v[120:121]
	v_med3_f32 v90, v90, -v96, v96
	v_med3_f32 v91, v91, -v96, v96
	v_med3_f32 v86, v86, -v96, v96
	v_med3_f32 v87, v87, -v96, v96
	v_med3_f32 v82, v82, -v96, v96
	v_med3_f32 v83, v83, -v96, v96
	v_add_co_u32_e32 v80, vcc, s56, v80
	v_cvt_pk_fp8_f32 v93, v90, v91 op_sel:[0,0,1]
	v_cvt_pk_fp8_f32 v94, v86, v87 op_sel:[0,0,1]
	v_cvt_pk_fp8_f32 v95, v82, v83 op_sel:[0,0,1]
	v_addc_co_u32_e32 v81, vcc, 0, v81, vcc
	s_nop 1
	v_permlane16_swap_b32 v92, v93
	v_permlane16_swap_b32 v94, v95
	s_nop 1
	v_permlane32_swap_b32 v92, v94
	v_permlane32_swap_b32 v93, v95
	global_store_dwordx4 v[80:81], v[92:95], off offset:512
	v_mov_b32_e32 v80, 0x43e00000
	v_pk_mul_f32 v[76:77], v[76:77], s[60:61] op_sel_hi:[1,0]
	v_pk_mul_f32 v[78:79], v[78:79], s[60:61] op_sel_hi:[1,0]
	v_med3_f32 v81, v76, -v80, v80
	v_med3_f32 v77, v77, -v80, v80
	s_nop 0
	v_cvt_pk_fp8_f32 v76, v81, v77
	v_med3_f32 v78, v78, -v80, v80
	v_med3_f32 v79, v79, -v80, v80
	v_pk_mul_f32 v[0:1], v[0:1], s[60:61] op_sel_hi:[1,0]
	v_cvt_pk_fp8_f32 v76, v78, v79 op_sel:[0,0,1]
	v_pk_mul_f32 v[72:73], v[72:73], s[60:61] op_sel_hi:[1,0]
	v_pk_mul_f32 v[4:5], v[4:5], s[60:61] op_sel_hi:[1,0]
	v_med3_f32 v0, v0, -v80, v80
	v_med3_f32 v1, v1, -v80, v80
	v_ashrrev_i32_e32 v123, 31, v122
	v_med3_f32 v72, v72, -v80, v80
	v_med3_f32 v73, v73, -v80, v80
	v_med3_f32 v4, v4, -v80, v80
	v_med3_f32 v5, v5, -v80, v80
	v_cvt_pk_fp8_f32 v79, v0, v1
	v_lshlrev_b64 v[0:1], 10, v[122:123]
	v_cvt_pk_fp8_f32 v77, v72, v73
	v_cvt_pk_fp8_f32 v78, v4, v5
	v_lshl_add_u64 v[0:1], s[86:87], 0, v[0:1]
	v_lshl_add_u64 v[0:1], v[0:1], 0, s[40:41]
	v_pk_mul_f32 v[74:75], v[74:75], s[60:61] op_sel_hi:[1,0]
	v_pk_mul_f32 v[6:7], v[6:7], s[60:61] op_sel_hi:[1,0]
	v_pk_mul_f32 v[2:3], v[2:3], s[60:61] op_sel_hi:[1,0]
	v_lshl_add_u64 v[0:1], v[0:1], 0, v[120:121]
	v_med3_f32 v74, v74, -v80, v80
	v_med3_f32 v75, v75, -v80, v80
	v_med3_f32 v6, v6, -v80, v80
	v_med3_f32 v7, v7, -v80, v80
	v_med3_f32 v2, v2, -v80, v80
	v_med3_f32 v3, v3, -v80, v80
	v_add_co_u32_e32 v0, vcc, 0x72000000, v0
	v_cvt_pk_fp8_f32 v77, v74, v75 op_sel:[0,0,1]
	v_cvt_pk_fp8_f32 v78, v6, v7 op_sel:[0,0,1]
	v_cvt_pk_fp8_f32 v79, v2, v3 op_sel:[0,0,1]
	v_addc_co_u32_e32 v1, vcc, 0, v1, vcc
	s_nop 1
	v_permlane16_swap_b32 v76, v77
	v_permlane16_swap_b32 v78, v79
	s_nop 1
	v_permlane32_swap_b32 v76, v78
	v_permlane32_swap_b32 v77, v79
	global_store_dwordx4 v[0:1], v[76:79], off offset:512

.LBB0_661:
	v_rcp_f32_e32 v97, v100
	v_mov_b32_e32 v99, 0x43e00000
	s_lshl_b32 s4, s74, 6
	v_mul_f32_e32 v98, 0x41000000, v97
	v_pk_mul_f32 v[92:93], v[92:93], v[98:99] op_sel_hi:[1,0]
	v_pk_mul_f32 v[94:95], v[94:95], v[98:99] op_sel_hi:[1,0]
	v_med3_f32 v97, v92, -v99, v99
	v_med3_f32 v93, v93, -v99, v99
	s_nop 0
	v_cvt_pk_fp8_f32 v92, v97, v93
	v_med3_f32 v93, v94, -v99, v99
	v_med3_f32 v94, v95, -v99, v99
	v_pk_mul_f32 v[84:85], v[84:85], v[98:99] op_sel_hi:[1,0]
	v_cvt_pk_fp8_f32 v92, v93, v94 op_sel:[0,0,1]
	v_med3_f32 v84, v84, -v99, v99
	v_med3_f32 v85, v85, -v99, v99
	s_nop 0
	v_cvt_pk_fp8_f32 v94, v84, v85
	v_pk_mul_f32 v[80:81], v[80:81], v[98:99] op_sel_hi:[1,0]
	v_pk_mul_f32 v[88:89], v[88:89], v[98:99] op_sel_hi:[1,0]
	v_med3_f32 v80, v80, -v99, v99
	v_med3_f32 v81, v81, -v99, v99
	v_med3_f32 v88, v88, -v99, v99
	v_med3_f32 v89, v89, -v99, v99
	v_pk_mul_f32 v[84:85], v[86:87], v[98:99] op_sel_hi:[1,0]
	v_cvt_pk_fp8_f32 v95, v80, v81
	v_cvt_pk_fp8_f32 v93, v88, v89
	v_med3_f32 v84, v84, -v99, v99
	v_med3_f32 v85, v85, -v99, v99
	s_add_u32 s4, s37, s4
	v_cvt_pk_fp8_f32 v94, v84, v85 op_sel:[0,0,1]
	v_pk_mul_f32 v[80:81], v[82:83], v[98:99] op_sel_hi:[1,0]
	v_rcp_f32_e32 v84, v96
	v_pk_mul_f32 v[88:89], v[90:91], v[98:99] op_sel_hi:[1,0]
	v_med3_f32 v80, v80, -v99, v99
	v_med3_f32 v81, v81, -v99, v99
	s_addc_u32 s5, s1, 0
	v_lshlrev_b32_e32 v184, 4, v157
	v_ashrrev_i32_e32 v159, 31, v158
	v_med3_f32 v88, v88, -v99, v99
	v_med3_f32 v89, v89, -v99, v99
	v_cvt_pk_fp8_f32 v95, v80, v81 op_sel:[0,0,1]
	v_lshl_add_u64 v[80:81], s[4:5], 0, v[184:185]
	v_lshlrev_b64 v[82:83], 10, v[158:159]
	v_cvt_pk_fp8_f32 v93, v88, v89 op_sel:[0,0,1]
	v_lshl_add_u64 v[82:83], v[80:81], 0, v[82:83]
	s_nop 1
	v_permlane16_swap_b32 v92, v93
	v_permlane16_swap_b32 v94, v95
	s_nop 1
	v_permlane32_swap_b32 v92, v94
	v_permlane32_swap_b32 v93, v95
	global_store_dwordx4 v[82:83], v[92:95], off
	v_mul_f32_e32 v82, 0x41000000, v84
	v_mov_b32_e32 v83, 0x43e00000
	v_ashrrev_i32_e32 v157, 31, v156
	v_pk_mul_f32 v[76:77], v[76:77], v[82:83] op_sel_hi:[1,0]
	v_pk_mul_f32 v[78:79], v[78:79], v[82:83] op_sel_hi:[1,0]
	v_med3_f32 v84, v76, -v83, v83
	v_med3_f32 v77, v77, -v83, v83
	s_nop 0
	v_cvt_pk_fp8_f32 v76, v84, v77
	v_pk_mul_f32 v[0:1], v[0:1], v[82:83] op_sel_hi:[1,0]
	v_med3_f32 v77, v78, -v83, v83
	v_med3_f32 v78, v79, -v83, v83
	v_pk_mul_f32 v[72:73], v[72:73], v[82:83] op_sel_hi:[1,0]
	v_pk_mul_f32 v[4:5], v[4:5], v[82:83] op_sel_hi:[1,0]
	v_med3_f32 v0, v0, -v83, v83
	v_med3_f32 v1, v1, -v83, v83
	v_cvt_pk_fp8_f32 v76, v77, v78 op_sel:[0,0,1]
	v_med3_f32 v72, v72, -v83, v83
	v_med3_f32 v73, v73, -v83, v83
	v_med3_f32 v4, v4, -v83, v83
	v_med3_f32 v5, v5, -v83, v83
	v_cvt_pk_fp8_f32 v79, v0, v1
	v_cvt_pk_fp8_f32 v77, v72, v73
	v_cvt_pk_fp8_f32 v78, v4, v5
	v_pk_mul_f32 v[0:1], v[2:3], v[82:83] op_sel_hi:[1,0]
	v_pk_mul_f32 v[72:73], v[74:75], v[82:83] op_sel_hi:[1,0]
	v_pk_mul_f32 v[4:5], v[6:7], v[82:83] op_sel_hi:[1,0]
	v_med3_f32 v0, v0, -v83, v83
	v_med3_f32 v1, v1, -v83, v83
	v_med3_f32 v72, v72, -v83, v83
	v_med3_f32 v73, v73, -v83, v83
	v_med3_f32 v4, v4, -v83, v83
	v_med3_f32 v5, v5, -v83, v83
	v_cvt_pk_fp8_f32 v79, v0, v1 op_sel:[0,0,1]
	v_lshlrev_b64 v[0:1], 10, v[156:157]
	v_cvt_pk_fp8_f32 v77, v72, v73 op_sel:[0,0,1]
	v_cvt_pk_fp8_f32 v78, v4, v5 op_sel:[0,0,1]
	v_lshl_add_u64 v[0:1], v[80:81], 0, v[0:1]
	s_mov_b64 s[10:11], 0
	s_nop 1
	v_permlane16_swap_b32 v76, v77
	v_permlane16_swap_b32 v78, v79
	s_nop 1
	v_permlane32_swap_b32 v76, v78
	v_permlane32_swap_b32 v77, v79
	global_store_dwordx4 v[0:1], v[76:79], off

.LBB0_884:
	v_lshl_add_u64 v[40:41], s[14:15], 0, v[130:131]
	s_brev_b32 s25, 44
	v_add_co_u32_e32 v42, vcc, s25, v40
	s_mov_b32 s25, 0x34008000
	s_nop 0
	v_addc_co_u32_e32 v43, vcc, 0, v41, vcc
	v_add_co_u32_e32 v40, vcc, s25, v40
	v_lshl_add_u64 v[52:53], s[14:15], 0, v[132:133]
	s_nop 0
	v_addc_co_u32_e32 v41, vcc, 0, v41, vcc
	s_mov_b32 s25, 0x500000
	global_load_dwordx4 v[60:63], v[42:43], off offset:64
	global_load_dwordx4 v[56:59], v[40:41], off offset:64
	v_add_co_u32_e32 v40, vcc, s25, v52
	s_mov_b32 s25, 0x540000
	s_nop 0
	v_addc_co_u32_e32 v41, vcc, 0, v53, vcc
	v_add_co_u32_e32 v44, vcc, s25, v52
	s_mov_b32 s25, 0x508000
	s_nop 0
	v_addc_co_u32_e32 v45, vcc, 0, v53, vcc
	v_add_co_u32_e32 v48, vcc, s25, v52
	s_mov_b32 s25, 0x548000
	s_nop 0
	v_addc_co_u32_e32 v49, vcc, 0, v53, vcc
	v_add_co_u32_e32 v52, vcc, s25, v52
	global_load_dwordx4 v[40:43], v[40:41], off offset:64
	s_nop 0
	v_addc_co_u32_e32 v53, vcc, 0, v53, vcc
	global_load_dwordx4 v[44:47], v[44:45], off offset:64
	s_waitcnt vmcnt(9)
	v_lshlrev_b32_e32 v80, 16, v20
	global_load_dwordx4 v[48:51], v[48:49], off offset:64
	v_and_b32_e32 v81, 0xffff0000, v20
	global_load_dwordx4 v[52:55], v[52:53], off offset:64
	ds_read_b128 v[72:75], v115
	ds_read_b128 v[64:67], v115 offset:16
	ds_read_b128 v[76:79], v115 offset:4096
	ds_read_b128 v[68:71], v115 offset:4112
	v_pk_mul_f32 v[80:81], v[128:129], v[80:81]
	v_lshlrev_b32_e32 v20, 16, v21
	v_and_b32_e32 v21, 0xffff0000, v21
	s_waitcnt lgkmcnt(1)
	v_pk_fma_f32 v[134:135], v[80:81], v[72:73], v[76:77]
	v_pk_mul_f32 v[20:21], v[128:129], v[20:21]
	v_cvt_pk_bf16_f32 v80, v134, v135
	v_lshlrev_b32_e32 v82, 16, v80
	v_and_b32_e32 v83, 0xffff0000, v80
	v_pk_fma_f32 v[20:21], v[20:21], v[74:75], v[78:79]
	v_pk_add_f32 v[82:83], v[134:135], v[82:83] neg_lo:[0,1] neg_hi:[0,1]
	v_cvt_pk_bf16_f32 v81, v20, v21
	v_cvt_pk_bf16_f32 v84, v82, v83
	v_lshlrev_b32_e32 v82, 16, v81
	v_and_b32_e32 v83, 0xffff0000, v81
	v_pk_add_f32 v[82:83], v[20:21], v[82:83] neg_lo:[0,1] neg_hi:[0,1]
	v_med3_f32 v119, v134, -v113, v113
	v_med3_f32 v134, v135, -v113, v113
	v_med3_f32 v135, v20, -v113, v113
	s_nop 0
	v_cvt_pk_fp8_f32 v20, v119, v134
	v_cvt_pk_bf16_f32 v85, v82, v83
	v_lshlrev_b32_e32 v82, 16, v22
	v_and_b32_e32 v83, 0xffff0000, v22
	v_pk_mul_f32 v[82:83], v[128:129], v[82:83]
	v_lshlrev_b32_e32 v22, 16, v23
	s_waitcnt lgkmcnt(0)
	v_pk_fma_f32 v[146:147], v[82:83], v[64:65], v[68:69]
	v_and_b32_e32 v23, 0xffff0000, v23
	v_med3_f32 v21, v21, -v113, v113
	v_pk_mul_f32 v[22:23], v[128:129], v[22:23]
	v_cvt_pk_fp8_f32 v20, v135, v21 op_sel:[0,0,1]
	v_med3_f32 v119, v146, -v113, v113
	v_med3_f32 v134, v147, -v113, v113
	s_nop 0
	v_pk_fma_f32 v[22:23], v[22:23], v[66:67], v[70:71]
	v_cvt_pk_fp8_f32 v21, v119, v134
	v_cvt_pk_bf16_f32 v83, v22, v23
	v_lshlrev_b32_e32 v148, 16, v83
	v_and_b32_e32 v149, 0xffff0000, v83
	v_pk_add_f32 v[148:149], v[22:23], v[148:149] neg_lo:[0,1] neg_hi:[0,1]
	v_med3_f32 v22, v22, -v113, v113
	v_med3_f32 v23, v23, -v113, v113
	v_cvt_pk_fp8_f32 v21, v22, v23 op_sel:[0,0,1]
	s_waitcnt vmcnt(10)
	v_lshlrev_b32_e32 v22, 16, v16
	v_and_b32_e32 v23, 0xffff0000, v16
	v_pk_mul_f32 v[22:23], v[126:127], v[22:23]
	v_cvt_pk_bf16_f32 v82, v146, v147
	v_pk_fma_f32 v[22:23], v[22:23], v[72:73], v[76:77]
	v_lshlrev_b32_e32 v76, 16, v17
	v_and_b32_e32 v77, 0xffff0000, v17
	v_pk_mul_f32 v[76:77], v[126:127], v[76:77]
	v_cvt_pk_bf16_f32 v16, v22, v23
	v_pk_fma_f32 v[76:77], v[76:77], v[74:75], v[78:79]
	v_lshlrev_b32_e32 v72, 16, v16
	v_cvt_pk_bf16_f32 v17, v76, v77
	v_and_b32_e32 v73, 0xffff0000, v16
	v_lshlrev_b32_e32 v74, 16, v17
	v_and_b32_e32 v75, 0xffff0000, v17
	v_pk_add_f32 v[72:73], v[22:23], v[72:73] neg_lo:[0,1] neg_hi:[0,1]
	v_pk_add_f32 v[74:75], v[76:77], v[74:75] neg_lo:[0,1] neg_hi:[0,1]
	v_cvt_pk_bf16_f32 v72, v72, v73
	v_cvt_pk_bf16_f32 v73, v74, v75
	v_lshlrev_b32_e32 v74, 16, v18
	v_and_b32_e32 v75, 0xffff0000, v18
	v_pk_mul_f32 v[74:75], v[126:127], v[74:75]
	s_waitcnt vmcnt(8)
	v_mfma_f32_16x16x32_bf16 v[36:39], v[0:3], v[80:83], v[36:39]
	v_fma_f32 v64, v74, v64, v68
	v_fma_f32 v65, v75, v65, v69
	v_lshlrev_b32_e32 v86, 16, v82
	v_cvt_pk_bf16_f32 v18, v64, v65
	v_lshlrev_b32_e32 v68, 16, v18
	v_and_b32_e32 v69, 0xffff0000, v18
	v_pk_add_f32 v[68:69], v[64:65], v[68:69] neg_lo:[0,1] neg_hi:[0,1]
	s_waitcnt vmcnt(8)
	v_mfma_f32_16x16x32_bf16 v[36:39], v[4:7], v[80:83], v[36:39]
	v_cvt_pk_bf16_f32 v74, v68, v69
	v_lshlrev_b32_e32 v68, 16, v19
	v_and_b32_e32 v69, 0xffff0000, v19
	v_pk_mul_f32 v[68:69], v[126:127], v[68:69]
	v_and_b32_e32 v87, 0xffff0000, v82
	v_pk_fma_f32 v[66:67], v[68:69], v[66:67], v[70:71]
	v_pk_add_f32 v[86:87], v[146:147], v[86:87] neg_lo:[0,1] neg_hi:[0,1]
	v_cvt_pk_bf16_f32 v19, v66, v67
	v_lshlrev_b32_e32 v68, 16, v19
	v_and_b32_e32 v69, 0xffff0000, v19
	v_mfma_f32_16x16x32_bf16 v[32:35], v[0:3], v[16:19], v[32:35]
	v_add_f32_e64 v68, v66, -v68
	v_add_f32_e64 v69, v67, -v69
	v_cvt_pk_bf16_f32 v86, v86, v87
	v_cvt_pk_bf16_f32 v87, v148, v149
	v_mfma_f32_16x16x32_bf16 v[4:7], v[4:7], v[16:19], v[32:35]
	v_cvt_pk_bf16_f32 v75, v68, v69
	v_med3_f32 v68, v22, -v113, v113
	v_med3_f32 v23, v23, -v113, v113
	v_mfma_f32_16x16x32_bf16 v[36:39], v[0:3], v[84:87], v[36:39]
	s_nop 0
	v_cvt_pk_fp8_f32 v22, v68, v23
	v_med3_f32 v64, v64, -v113, v113
	v_mfma_f32_16x16x32_bf16 v[32:35], v[0:3], v[72:75], v[4:7]
	v_med3_f32 v65, v65, -v113, v113
	s_nop 0
	v_cvt_pk_fp8_f32 v23, v64, v65
	s_waitcnt vmcnt(7)
	v_mfma_f32_16x16x32_bf16 v[0:3], v[8:11], v[16:19], v[24:27]
	v_med3_f32 v66, v66, -v113, v113
	s_mov_b32 s25, 0xdd000000
	v_med3_f32 v69, v76, -v113, v113
	s_waitcnt vmcnt(6)
	v_mfma_f32_16x16x32_bf16 v[0:3], v[12:15], v[16:19], v[0:3]
	v_med3_f32 v70, v77, -v113, v113
	v_cvt_pk_fp8_f32 v22, v69, v70 op_sel:[0,0,1]
	v_mov_b32_e32 v119, v185
	v_mfma_f32_16x16x32_bf16 v[28:31], v[8:11], v[80:83], v[28:31]
	s_nop 1
	v_permlane16_swap_b32 v20, v22
	v_lshl_add_u64 v[132:133], v[132:133], 0, s[46:47]
	v_lshl_add_u64 v[130:131], v[130:131], 0, s[46:47]
	v_mfma_f32_16x16x32_bf16 v[24:27], v[8:11], v[72:75], v[0:3]
	s_nop 2
	v_med3_f32 v0, v67, -v113, v113
	v_cvt_pk_fp8_f32 v23, v66, v0 op_sel:[0,0,1]
	v_lshl_add_u64 v[0:1], s[14:15], 0, v[124:125]
	v_mfma_f32_16x16x32_bf16 v[28:31], v[12:15], v[80:83], v[28:31]
	v_add_co_u32_e32 v134, vcc, s25, v0
	s_and_b32 s25, s24, 0x3c0
	s_lshl_b32 s40, s25, 1
	v_addc_co_u32_e32 v135, vcc, 0, v1, vcc
	v_lshl_add_u64 v[12:13], v[100:101], 0, s[40:41]
	s_nop 1
	v_permlane16_swap_b32 v21, v23
	global_store_dwordx4 v[134:135], v[20:23], off
	v_lshl_add_u64 v[0:1], v[120:121], 0, s[40:41]
	v_lshl_add_u64 v[4:5], v[12:13], 0, v[184:185]
	v_mfma_f32_16x16x32_bf16 v[28:31], v[8:11], v[84:87], v[28:31]
	global_load_dwordx4 v[20:23], v[0:1], off
	v_lshl_add_u64 v[8:9], v[98:99], 0, s[40:41]
	global_load_dwordx4 v[4:7], v[4:5], off
	v_lshl_add_u64 v[0:1], v[122:123], 0, s[40:41]
	v_lshl_add_u64 v[12:13], v[12:13], 0, v[118:119]
	global_load_dwordx4 v[16:19], v[0:1], off
	s_waitcnt vmcnt(9)
	v_lshlrev_b32_e32 v80, 16, v60
	global_load_dwordx4 v[12:15], v[12:13], off
	v_lshl_add_u64 v[0:1], v[8:9], 0, v[184:185]
	v_lshl_add_u64 v[8:9], v[8:9], 0, v[118:119]
	global_load_dwordx4 v[0:3], v[0:1], off
	v_and_b32_e32 v81, 0xffff0000, v60
	global_load_dwordx4 v[8:11], v[8:9], off
	ds_read_b128 v[72:75], v115 offset:128
	ds_read_b128 v[64:67], v115 offset:144
	ds_read_b128 v[76:79], v115 offset:4224
	ds_read_b128 v[68:71], v115 offset:4240
	v_pk_mul_f32 v[80:81], v[128:129], v[80:81]
	v_lshlrev_b32_e32 v60, 16, v61
	v_and_b32_e32 v61, 0xffff0000, v61
	s_waitcnt lgkmcnt(1)
	v_pk_fma_f32 v[146:147], v[80:81], v[72:73], v[76:77]
	v_pk_mul_f32 v[60:61], v[128:129], v[60:61]
	v_cvt_pk_bf16_f32 v80, v146, v147
	v_lshlrev_b32_e32 v82, 16, v80
	v_and_b32_e32 v83, 0xffff0000, v80
	v_pk_fma_f32 v[60:61], v[60:61], v[74:75], v[78:79]
	v_pk_add_f32 v[82:83], v[146:147], v[82:83] neg_lo:[0,1] neg_hi:[0,1]
	v_cvt_pk_bf16_f32 v81, v60, v61
	v_cvt_pk_bf16_f32 v84, v82, v83
	v_lshlrev_b32_e32 v82, 16, v81
	v_and_b32_e32 v83, 0xffff0000, v81
	v_pk_add_f32 v[82:83], v[60:61], v[82:83] neg_lo:[0,1] neg_hi:[0,1]
	v_med3_f32 v119, v146, -v113, v113
	v_med3_f32 v145, v147, -v113, v113
	v_med3_f32 v146, v60, -v113, v113
	s_nop 0
	v_cvt_pk_fp8_f32 v60, v119, v145
	v_cvt_pk_bf16_f32 v85, v82, v83
	v_lshlrev_b32_e32 v82, 16, v62
	v_and_b32_e32 v83, 0xffff0000, v62
	v_pk_mul_f32 v[82:83], v[128:129], v[82:83]
	v_lshlrev_b32_e32 v62, 16, v63
	s_waitcnt lgkmcnt(0)
	v_pk_fma_f32 v[148:149], v[82:83], v[64:65], v[68:69]
	v_and_b32_e32 v63, 0xffff0000, v63
	v_med3_f32 v61, v61, -v113, v113
	v_pk_mul_f32 v[62:63], v[128:129], v[62:63]
	v_cvt_pk_fp8_f32 v60, v146, v61 op_sel:[0,0,1]
	v_med3_f32 v119, v148, -v113, v113
	v_med3_f32 v145, v149, -v113, v113
	s_nop 0
	v_pk_fma_f32 v[62:63], v[62:63], v[66:67], v[70:71]
	v_cvt_pk_fp8_f32 v61, v119, v145
	v_cvt_pk_bf16_f32 v83, v62, v63
	v_lshlrev_b32_e32 v150, 16, v83
	v_and_b32_e32 v151, 0xffff0000, v83
	v_pk_add_f32 v[150:151], v[62:63], v[150:151] neg_lo:[0,1] neg_hi:[0,1]
	v_med3_f32 v62, v62, -v113, v113
	v_med3_f32 v63, v63, -v113, v113
	v_cvt_pk_fp8_f32 v61, v62, v63 op_sel:[0,0,1]
	s_waitcnt vmcnt(11)
	v_lshlrev_b32_e32 v62, 16, v56
	v_and_b32_e32 v63, 0xffff0000, v56
	v_pk_mul_f32 v[62:63], v[126:127], v[62:63]
	v_cvt_pk_bf16_f32 v82, v148, v149
	v_pk_fma_f32 v[62:63], v[62:63], v[72:73], v[76:77]
	v_lshlrev_b32_e32 v76, 16, v57
	v_and_b32_e32 v77, 0xffff0000, v57
	v_pk_mul_f32 v[76:77], v[126:127], v[76:77]
	v_cvt_pk_bf16_f32 v56, v62, v63
	v_pk_fma_f32 v[76:77], v[76:77], v[74:75], v[78:79]
	v_lshlrev_b32_e32 v72, 16, v56
	v_cvt_pk_bf16_f32 v57, v76, v77
	v_and_b32_e32 v73, 0xffff0000, v56
	v_lshlrev_b32_e32 v74, 16, v57
	v_and_b32_e32 v75, 0xffff0000, v57
	v_pk_add_f32 v[72:73], v[62:63], v[72:73] neg_lo:[0,1] neg_hi:[0,1]
	v_pk_add_f32 v[74:75], v[76:77], v[74:75] neg_lo:[0,1] neg_hi:[0,1]
	v_cvt_pk_bf16_f32 v72, v72, v73
	v_cvt_pk_bf16_f32 v73, v74, v75
	v_lshlrev_b32_e32 v74, 16, v58
	v_and_b32_e32 v75, 0xffff0000, v58
	v_pk_mul_f32 v[74:75], v[126:127], v[74:75]
	s_waitcnt vmcnt(10)
	v_mfma_f32_16x16x32_bf16 v[36:39], v[40:43], v[80:83], v[36:39]
	v_fma_f32 v68, v74, v64, v68
	v_fma_f32 v69, v75, v65, v69
	v_med3_f32 v63, v63, -v113, v113
	v_cvt_pk_bf16_f32 v58, v68, v69
	v_lshlrev_b32_e32 v64, 16, v58
	v_and_b32_e32 v65, 0xffff0000, v58
	v_pk_add_f32 v[64:65], v[68:69], v[64:65] neg_lo:[0,1] neg_hi:[0,1]
	s_waitcnt vmcnt(8)
	v_mfma_f32_16x16x32_bf16 v[28:31], v[48:51], v[80:83], v[28:31]
	v_cvt_pk_bf16_f32 v74, v64, v65
	v_lshlrev_b32_e32 v64, 16, v59
	v_and_b32_e32 v65, 0xffff0000, v59
	v_pk_mul_f32 v[64:65], v[126:127], v[64:65]
	v_mfma_f32_16x16x32_bf16 v[36:39], v[44:47], v[80:83], v[36:39]
	v_fma_f32 v64, v64, v66, v70
	v_fma_f32 v65, v65, v67, v71
	v_lshlrev_b32_e32 v86, 16, v82
	v_cvt_pk_bf16_f32 v59, v64, v65
	v_lshlrev_b32_e32 v66, 16, v59
	v_and_b32_e32 v67, 0xffff0000, v59
	v_pk_add_f32 v[66:67], v[64:65], v[66:67] neg_lo:[0,1] neg_hi:[0,1]
	v_mfma_f32_16x16x32_bf16 v[32:35], v[40:43], v[56:59], v[32:35]
	v_cvt_pk_bf16_f32 v75, v66, v67
	v_med3_f32 v66, v62, -v113, v113
	s_nop 0
	v_mfma_f32_16x16x32_bf16 v[24:27], v[48:51], v[56:59], v[24:27]
	v_cvt_pk_fp8_f32 v62, v66, v63
	v_and_b32_e32 v87, 0xffff0000, v82
	v_med3_f32 v67, v76, -v113, v113
	s_waitcnt vmcnt(7)
	v_mfma_f32_16x16x32_bf16 v[28:31], v[52:55], v[80:83], v[28:31]
	v_med3_f32 v70, v77, -v113, v113
	v_pk_add_f32 v[86:87], v[148:149], v[86:87] neg_lo:[0,1] neg_hi:[0,1]
	v_cvt_pk_fp8_f32 v62, v67, v70 op_sel:[0,0,1]
	v_mfma_f32_16x16x32_bf16 v[32:35], v[44:47], v[56:59], v[32:35]
	v_med3_f32 v66, v68, -v113, v113
	v_med3_f32 v67, v69, -v113, v113
	s_nop 0
	v_mfma_f32_16x16x32_bf16 v[24:27], v[52:55], v[56:59], v[24:27]
	v_cvt_pk_bf16_f32 v86, v86, v87
	v_cvt_pk_bf16_f32 v87, v150, v151
	v_cvt_pk_fp8_f32 v63, v66, v67
	v_mfma_f32_16x16x32_bf16 v[32:35], v[40:43], v[72:75], v[32:35]
	v_med3_f32 v64, v64, -v113, v113
	s_add_i32 s24, s24, 64
	v_add_u32_e32 v115, 0x100, v115
	v_mfma_f32_16x16x32_bf16 v[36:39], v[40:43], v[84:87], v[36:39]
	v_med3_f32 v40, v65, -v113, v113
	v_cvt_pk_fp8_f32 v63, v64, v40 op_sel:[0,0,1]
	v_lshl_add_u64 v[124:125], v[124:125], 0, 64
	v_mfma_f32_16x16x32_bf16 v[28:31], v[48:51], v[84:87], v[28:31]
	s_cmpk_eq_i32 s24, 0x440
	s_nop 1
	v_permlane16_swap_b32 v60, v62
	s_nop 1
	v_permlane16_swap_b32 v61, v63
	v_mfma_f32_16x16x32_bf16 v[24:27], v[48:51], v[72:75], v[24:27]
	global_store_dwordx4 v[134:135], v[60:63], off offset:32
	s_cbranch_scc0 .LBB0_884
	s_load_dwordx2 s[24:25], s[12:13], 0x70
	s_waitcnt vmcnt(5) lgkmcnt(0)
	v_lshl_add_u64 v[4:5], v[110:111], 2, s[24:25]
	global_load_dwordx4 v[0:3], v[4:5], off
	s_waitcnt vmcnt(0)
	v_pk_add_f32 v[6:7], v[36:37], v[0:1]
	ds_write2_b32 v138, v6, v7 offset1:1
	v_pk_add_f32 v[6:7], v[38:39], v[2:3]
	ds_write2_b32 v138, v6, v7 offset0:2 offset1:3
	global_load_dwordx4 v[4:7], v[4:5], off offset:64
	v_pk_add_f32 v[0:1], v[32:33], v[0:1]
	s_waitcnt vmcnt(0)
	v_pk_add_f32 v[8:9], v[28:29], v[4:5]
	ds_write2_b32 v138, v8, v9 offset0:16 offset1:17
	v_pk_add_f32 v[8:9], v[30:31], v[6:7]
	ds_write2_b32 v138, v8, v9 offset0:18 offset1:19
	v_add_u32_e32 v8, 0x840, v138
	ds_write2_b32 v8, v0, v1 offset1:1
	v_pk_add_f32 v[0:1], v[34:35], v[2:3]
	v_add_u32_e32 v2, 0x848, v138
	ds_write2_b32 v2, v0, v1 offset1:1
	v_pk_add_f32 v[0:1], v[24:25], v[4:5]
	v_add_u32_e32 v2, 0x880, v138
	ds_write2_b32 v2, v0, v1 offset1:1
	v_pk_add_f32 v[0:1], v[26:27], v[6:7]
	v_add_u32_e32 v2, 0x888, v138
	ds_write2_b32 v2, v0, v1 offset1:1
	s_waitcnt lgkmcnt(0)
	s_and_saveexec_b64 s[24:25], s[2:3]
	s_cbranch_execz .LBB0_900
	v_mov_b32_e32 v5, 0
	v_mov_b32_e32 v11, 0xff800000
	s_mov_b32 s40, 0
	v_mov_b32_e32 v6, 0xff800000
	v_mov_b32_e32 v8, 0xff800000
	v_mov_b32_e32 v9, 0xff800000
	v_mov_b32_e32 v7, 0
	v_mov_b32_e32 v2, 0
	v_mov_b32_e32 v3, 0

.LBB0_1041:
	s_ashr_i32 s29, s28, 31
	s_lshl_b64 s[24:25], s[28:29], 2
	s_add_u32 s24, s38, s24
	s_addc_u32 s25, s39, s25
	v_mov_b32_e32 v40, v152
	global_load_dword v155, v185, s[24:25]
	s_lshl_b32 s19, s28, 8
	v_lshrrev_b32_e32 v40, 10, v40
	v_add_u32_e32 v40, s19, v40
	v_ashrrev_i32_e32 v41, 31, v40
	v_lshl_add_u64 v[40:41], v[40:41], 2, s[6:7]
	global_load_dword v156, v[40:41], off
	v_mov_b32_e32 v40, v153
	s_nop 0
	v_lshrrev_b32_e32 v40, 10, v40
	v_add_u32_e32 v40, s19, v40
	v_ashrrev_i32_e32 v41, 31, v40
	v_lshl_add_u64 v[40:41], v[40:41], 2, s[6:7]
	global_load_dword v157, v[40:41], off
	v_mov_b32_e32 v40, v152
	s_bitset1_b32 s19, 7
	v_lshrrev_b32_e32 v40, 10, v40
	v_add_u32_e32 v40, s19, v40
	v_ashrrev_i32_e32 v41, 31, v40
	v_lshl_add_u64 v[40:41], v[40:41], 2, s[6:7]
	global_load_dword v158, v[40:41], off
	v_mov_b32_e32 v40, v153
	s_nop 0
	v_lshrrev_b32_e32 v40, 10, v40
	v_add_u32_e32 v40, s19, v40
	v_ashrrev_i32_e32 v41, 31, v40
	v_lshl_add_u64 v[40:41], v[40:41], 2, s[6:7]
	s_mov_b32 s19, s61
	global_load_dword v159, v[40:41], off
	v_mbcnt_lo_u32_b32 v40, -1, 0
	v_mbcnt_hi_u32_b32 v40, -1, v40
	s_lshl_b32 s19, s19, 6
	v_mov_b32_e32 v41, 0xff
	v_bitop3_b32 v40, s19, v41, v40 bitop3:0xc8
	s_movk_i32 s19, 0x80
	v_cmp_gt_u32_e32 vcc, s19, v40
	s_lshl_b32 s19, s26, 7
	v_or_b32_e32 v41, s19, v40
	s_addk_i32 s19, 0x380
	v_add_u32_e32 v40, s19, v40
	s_ashr_i32 s19, s18, 31
	s_lshl_b64 s[24:25], s[18:19], 13
	v_cndmask_b32_e32 v40, v40, v41, vcc
	s_add_u32 s24, s68, s24
	v_ashrrev_i32_e32 v41, 31, v40
	s_addc_u32 s25, s70, s25
	v_lshl_add_u64 v[40:41], v[40:41], 2, s[24:25]
	s_mov_b32 s19, s61
	global_load_dword v160, v[40:41], off
	v_mbcnt_lo_u32_b32 v161, -1, 0
	v_mbcnt_hi_u32_b32 v161, -1, v161
	s_lshl_b32 s24, s72, 10
	v_lshl_or_b32 v40, s19, 6, v161
	s_and_b32 s24, s24, 0x400
	v_readfirstlane_b32 s19, v40
	s_lshr_b32 s25, s19, 1
	s_and_b32 s25, s25, 0x60
	s_add_i32 s24, s24, 0
	s_lshl_b32 s29, s25, 2
	s_add_i32 s24, s24, s29
	s_lshl_b32 s29, s34, 7
	v_lshrrev_b32_e32 v40, 1, v161
	v_lshlrev_b32_e32 v163, 1, v161
	v_and_or_b32 v162, v40, 16, s29
	v_and_b32_e32 v40, 0x60, v163
	v_add_u32_e32 v40, s24, v40
	v_add_u32_e32 v140, 0x23000, v40
	ds_read_b128 v[52:55], v140
	ds_read_b128 v[40:43], v140 offset:16
	ds_read_b128 v[136:139], v140 offset:512
	s_lshl_b32 s24, s30, 8
	s_mov_b32 s30, 0xc01d265f
	s_waitcnt lgkmcnt(0)
	v_pk_fma_f32 v[132:133], v[132:133], s[48:49], v[52:53] op_sel_hi:[1,0,1]
	s_ashr_i32 s19, s19, 2
	v_pk_fma_f32 v[144:145], v[138:139], 4.0, 4.0 op_sel_hi:[1,0,0]
	v_pk_fma_f32 v[146:147], v[136:137], 4.0, 4.0 op_sel_hi:[1,0,0]
	ds_read_b128 v[136:139], v140 offset:528
	v_min_f32_e32 v132, 0x40e00000, v132
	v_min_f32_e32 v133, 0x40e00000, v133
	s_andn2_b32 s19, s19, 63
	s_add_i32 s19, s19, s24
	s_waitcnt lgkmcnt(0)
	v_pk_fma_f32 v[142:143], v[138:139], 4.0, 4.0 op_sel_hi:[1,0,0]
	v_and_b32_e32 v138, 3, v161
	v_pk_fma_f32 v[140:141], v[136:137], 4.0, 4.0 op_sel_hi:[1,0,0]
	v_or_b32_e32 v136, s25, v162
	v_and_or_b32 v138, v163, 24, v138
	v_pk_mul_f32 v[162:163], v[132:133], s[30:31] op_sel_hi:[1,0]
	v_lshrrev_b32_e32 v137, 2, v161
	v_exp_f32_e32 v162, v162
	v_exp_f32_e32 v163, v163
	v_and_b32_e32 v137, 4, v137
	s_mov_b32 s24, 0x3d800000
	v_or3_b32 v138, v138, v137, s19
	v_pk_add_f32 v[162:163], v[162:163], 1.0 op_sel_hi:[1,0]
	v_pk_fma_f32 v[128:129], v[128:129], s[24:25], v[146:147] op_sel_hi:[1,0,1]
	v_rcp_f32_e32 v162, v162
	v_rcp_f32_e32 v163, v163
	s_mov_b32 s19, 0xc1c00000
	v_mov_b32_e32 v161, 0x42000000
	v_pk_fma_f32 v[134:135], v[134:135], s[48:49], v[54:55] op_sel_hi:[1,0,1]
	v_med3_f32 v128, v128, s19, v161
	v_med3_f32 v129, v129, s19, v161
	v_pk_mul_f32 v[132:133], v[132:133], v[162:163]
	v_pk_fma_f32 v[130:131], v[130:131], s[24:25], v[144:145] op_sel_hi:[1,0,1]
	v_pk_mul_f32 v[132:133], v[128:129], v[132:133]
	v_min_f32_e32 v128, 0x40e00000, v134
	v_min_f32_e32 v129, 0x40e00000, v135
	v_pk_mul_f32 v[134:135], v[128:129], s[30:31] op_sel_hi:[1,0]
	v_med3_f32 v130, v130, s19, v161
	v_exp_f32_e32 v134, v134
	v_exp_f32_e32 v135, v135
	v_med3_f32 v131, v131, s19, v161
	v_pk_fma_f32 v[124:125], v[124:125], s[48:49], v[40:41] op_sel_hi:[1,0,1]
	v_pk_fma_f32 v[120:121], v[120:121], s[24:25], v[140:141] op_sel_hi:[1,0,1]
	v_pk_add_f32 v[134:135], v[134:135], 1.0 op_sel_hi:[1,0]
	v_min_f32_e32 v124, 0x40e00000, v124
	v_rcp_f32_e32 v134, v134
	v_rcp_f32_e32 v135, v135
	v_min_f32_e32 v125, 0x40e00000, v125
	v_med3_f32 v120, v120, s19, v161
	v_med3_f32 v121, v121, s19, v161
	v_pk_mul_f32 v[128:129], v[128:129], v[134:135]
	v_pk_fma_f32 v[116:117], v[116:117], s[48:49], v[52:53] op_sel_hi:[1,0,1]
	v_pk_mul_f32 v[130:131], v[130:131], v[128:129]
	v_cvt_pk_fp8_f32 v128, v132, v133
	v_min_f32_e32 v116, 0x40e00000, v116
	v_min_f32_e32 v117, 0x40e00000, v117
	v_cvt_pk_fp8_f32 v128, v130, v131 op_sel:[0,0,1]
	v_pk_mul_f32 v[130:131], v[124:125], s[30:31] op_sel_hi:[1,0]
	v_pk_fma_f32 v[112:113], v[112:113], s[24:25], v[146:147] op_sel_hi:[1,0,1]
	v_exp_f32_e32 v130, v130
	v_exp_f32_e32 v131, v131
	v_med3_f32 v112, v112, s19, v161
	v_med3_f32 v113, v113, s19, v161
	v_pk_fma_f32 v[108:109], v[108:109], s[48:49], v[40:41] op_sel_hi:[1,0,1]
	v_pk_add_f32 v[130:131], v[130:131], 1.0 op_sel_hi:[1,0]
	v_min_f32_e32 v108, 0x40e00000, v108
	v_rcp_f32_e32 v130, v130
	v_rcp_f32_e32 v131, v131
	v_min_f32_e32 v109, 0x40e00000, v109
	v_pk_fma_f32 v[104:105], v[104:105], s[24:25], v[140:141] op_sel_hi:[1,0,1]
	v_pk_fma_f32 v[126:127], v[126:127], s[48:49], v[42:43] op_sel_hi:[1,0,1]
	v_pk_mul_f32 v[124:125], v[124:125], v[130:131]
	s_nop 0
	v_pk_mul_f32 v[120:121], v[120:121], v[124:125]
	v_pk_fma_f32 v[118:119], v[118:119], s[48:49], v[54:55] op_sel_hi:[1,0,1]
	v_cvt_pk_fp8_f32 v129, v120, v121
	v_pk_mul_f32 v[120:121], v[116:117], s[30:31] op_sel_hi:[1,0]
	v_pk_fma_f32 v[110:111], v[110:111], s[48:49], v[42:43] op_sel_hi:[1,0,1]
	v_exp_f32_e32 v120, v120
	v_exp_f32_e32 v121, v121
	v_med3_f32 v104, v104, s19, v161
	v_med3_f32 v105, v105, s19, v161
	v_min_f32_e32 v124, 0x40e00000, v126
	v_pk_add_f32 v[120:121], v[120:121], 1.0 op_sel_hi:[1,0]
	v_min_f32_e32 v125, 0x40e00000, v127
	v_rcp_f32_e32 v120, v120
	v_rcp_f32_e32 v121, v121
	v_pk_mul_f32 v[126:127], v[124:125], s[30:31] op_sel_hi:[1,0]
	s_nop 0
	v_exp_f32_e32 v126, v126
	v_pk_mul_f32 v[116:117], v[116:117], v[120:121]
	v_exp_f32_e32 v127, v127
	v_pk_mul_f32 v[112:113], v[112:113], v[116:117]
	v_min_f32_e32 v116, 0x40e00000, v118
	v_cvt_pk_fp8_f32 v130, v112, v113
	v_pk_mul_f32 v[112:113], v[108:109], s[30:31] op_sel_hi:[1,0]
	v_min_f32_e32 v117, 0x40e00000, v119
	v_exp_f32_e32 v112, v112
	v_exp_f32_e32 v113, v113
	v_pk_mul_f32 v[118:119], v[116:117], s[30:31] op_sel_hi:[1,0]
	v_pk_add_f32 v[126:127], v[126:127], 1.0 op_sel_hi:[1,0]
	v_exp_f32_e32 v118, v118
	v_pk_add_f32 v[112:113], v[112:113], 1.0 op_sel_hi:[1,0]
	v_exp_f32_e32 v119, v119
	v_rcp_f32_e32 v112, v112
	v_rcp_f32_e32 v113, v113
	v_rcp_f32_e32 v126, v126
	v_pk_add_f32 v[118:119], v[118:119], 1.0 op_sel_hi:[1,0]
	v_rcp_f32_e32 v127, v127
	v_pk_mul_f32 v[108:109], v[108:109], v[112:113]
	v_rcp_f32_e32 v118, v118
	v_pk_mul_f32 v[104:105], v[104:105], v[108:109]
	v_min_f32_e32 v108, 0x40e00000, v110
	v_min_f32_e32 v109, 0x40e00000, v111
	v_pk_mul_f32 v[110:111], v[108:109], s[30:31] op_sel_hi:[1,0]
	v_rcp_f32_e32 v119, v119
	v_exp_f32_e32 v110, v110
	v_exp_f32_e32 v111, v111
	v_cvt_pk_fp8_f32 v131, v104, v105
	v_pk_fma_f32 v[122:123], v[122:123], s[24:25], v[142:143] op_sel_hi:[1,0,1]
	v_pk_fma_f32 v[114:115], v[114:115], s[24:25], v[144:145] op_sel_hi:[1,0,1]
	v_pk_add_f32 v[110:111], v[110:111], 1.0 op_sel_hi:[1,0]
	v_pk_fma_f32 v[106:107], v[106:107], s[24:25], v[142:143] op_sel_hi:[1,0,1]
	v_rcp_f32_e32 v110, v110
	v_rcp_f32_e32 v111, v111
	v_ashrrev_i32_e32 v139, 31, v138
	v_med3_f32 v122, v122, s19, v161
	v_med3_f32 v123, v123, s19, v161
	v_pk_mul_f32 v[124:125], v[124:125], v[126:127]
	v_med3_f32 v114, v114, s19, v161
	v_med3_f32 v115, v115, s19, v161
	v_pk_mul_f32 v[116:117], v[116:117], v[118:119]
	v_med3_f32 v106, v106, s19, v161
	v_med3_f32 v107, v107, s19, v161
	v_pk_mul_f32 v[108:109], v[108:109], v[110:111]
	v_lshlrev_b64 v[104:105], 10, v[138:139]
	v_ashrrev_i32_e32 v137, 31, v136
	v_pk_mul_f32 v[122:123], v[122:123], v[124:125]
	v_pk_mul_f32 v[114:115], v[114:115], v[116:117]
	v_pk_mul_f32 v[106:107], v[106:107], v[108:109]
	v_lshl_add_u64 v[104:105], s[16:17], 0, v[104:105]
	v_pk_fma_f32 v[100:101], v[100:101], s[48:49], v[52:53] op_sel_hi:[1,0,1]
	v_cvt_pk_fp8_f32 v129, v122, v123 op_sel:[0,0,1]
	v_cvt_pk_fp8_f32 v130, v114, v115 op_sel:[0,0,1]
	v_cvt_pk_fp8_f32 v131, v106, v107 op_sel:[0,0,1]
	v_lshl_add_u64 v[104:105], v[104:105], 0, v[136:137]
	v_min_f32_e32 v100, 0x40e00000, v100
	v_min_f32_e32 v101, 0x40e00000, v101
	s_nop 1
	v_permlane16_swap_b32 v128, v130
	s_nop 1
	v_permlane16_swap_b32 v129, v131
	global_store_dwordx4 v[104:105], v[128:131], off
	v_pk_mul_f32 v[104:105], v[100:101], s[30:31] op_sel_hi:[1,0]
	v_pk_fma_f32 v[96:97], v[96:97], s[24:25], v[146:147] op_sel_hi:[1,0,1]
	v_exp_f32_e32 v104, v104
	v_exp_f32_e32 v105, v105
	v_pk_fma_f32 v[102:103], v[102:103], s[48:49], v[54:55] op_sel_hi:[1,0,1]
	v_med3_f32 v96, v96, s19, v161
	v_med3_f32 v97, v97, s19, v161
	v_pk_add_f32 v[104:105], v[104:105], 1.0 op_sel_hi:[1,0]
	v_pk_fma_f32 v[98:99], v[98:99], s[24:25], v[144:145] op_sel_hi:[1,0,1]
	v_rcp_f32_e32 v104, v104
	v_rcp_f32_e32 v105, v105
	v_med3_f32 v98, v98, s19, v161
	v_med3_f32 v99, v99, s19, v161
	v_pk_fma_f32 v[92:93], v[92:93], s[48:49], v[40:41] op_sel_hi:[1,0,1]
	v_pk_mul_f32 v[100:101], v[100:101], v[104:105]
	v_min_f32_e32 v92, 0x40e00000, v92
	v_pk_mul_f32 v[100:101], v[96:97], v[100:101]
	v_min_f32_e32 v96, 0x40e00000, v102
	v_min_f32_e32 v97, 0x40e00000, v103
	v_pk_mul_f32 v[102:103], v[96:97], s[30:31] op_sel_hi:[1,0]
	v_min_f32_e32 v93, 0x40e00000, v93
	v_exp_f32_e32 v102, v102
	v_exp_f32_e32 v103, v103
	v_pk_fma_f32 v[88:89], v[88:89], s[24:25], v[140:141] op_sel_hi:[1,0,1]
	v_pk_fma_f32 v[84:85], v[84:85], s[48:49], v[52:53] op_sel_hi:[1,0,1]
	v_med3_f32 v88, v88, s19, v161
	v_pk_add_f32 v[102:103], v[102:103], 1.0 op_sel_hi:[1,0]
	v_med3_f32 v89, v89, s19, v161
	v_rcp_f32_e32 v102, v102
	v_rcp_f32_e32 v103, v103
	v_min_f32_e32 v84, 0x40e00000, v84
	v_min_f32_e32 v85, 0x40e00000, v85
	v_pk_fma_f32 v[80:81], v[80:81], s[24:25], v[146:147] op_sel_hi:[1,0,1]
	v_pk_mul_f32 v[96:97], v[96:97], v[102:103]
	v_med3_f32 v80, v80, s19, v161
	v_pk_mul_f32 v[98:99], v[98:99], v[96:97]
	v_cvt_pk_fp8_f32 v96, v100, v101
	v_med3_f32 v81, v81, s19, v161
	v_pk_fma_f32 v[76:77], v[76:77], s[48:49], v[40:41] op_sel_hi:[1,0,1]
	v_cvt_pk_fp8_f32 v96, v98, v99 op_sel:[0,0,1]
	v_pk_mul_f32 v[98:99], v[92:93], s[30:31] op_sel_hi:[1,0]
	v_min_f32_e32 v76, 0x40e00000, v76
	v_exp_f32_e32 v98, v98
	v_exp_f32_e32 v99, v99
	v_min_f32_e32 v77, 0x40e00000, v77
	v_pk_fma_f32 v[72:73], v[72:73], s[24:25], v[140:141] op_sel_hi:[1,0,1]
	v_pk_fma_f32 v[78:79], v[78:79], s[48:49], v[42:43] op_sel_hi:[1,0,1]
	v_pk_add_f32 v[98:99], v[98:99], 1.0 op_sel_hi:[1,0]
	v_med3_f32 v72, v72, s19, v161
	v_rcp_f32_e32 v98, v98
	v_rcp_f32_e32 v99, v99
	v_med3_f32 v73, v73, s19, v161
	v_pk_fma_f32 v[74:75], v[74:75], s[24:25], v[142:143] op_sel_hi:[1,0,1]
	v_pk_fma_f32 v[68:69], v[68:69], s[48:49], v[52:53] op_sel_hi:[1,0,1]
	v_pk_mul_f32 v[92:93], v[92:93], v[98:99]
	s_nop 0
	v_pk_mul_f32 v[88:89], v[88:89], v[92:93]
	s_nop 0
	v_cvt_pk_fp8_f32 v97, v88, v89
	v_pk_mul_f32 v[88:89], v[84:85], s[30:31] op_sel_hi:[1,0]
	v_med3_f32 v74, v74, s19, v161
	v_exp_f32_e32 v88, v88
	v_exp_f32_e32 v89, v89
	v_med3_f32 v75, v75, s19, v161
	v_min_f32_e32 v68, 0x40e00000, v68
	v_min_f32_e32 v69, 0x40e00000, v69
	v_pk_add_f32 v[88:89], v[88:89], 1.0 op_sel_hi:[1,0]
	v_pk_fma_f32 v[64:65], v[64:65], s[24:25], v[146:147] op_sel_hi:[1,0,1]
	v_rcp_f32_e32 v88, v88
	v_rcp_f32_e32 v89, v89
	v_pk_fma_f32 v[70:71], v[70:71], s[48:49], v[54:55] op_sel_hi:[1,0,1]
	v_med3_f32 v64, v64, s19, v161
	v_med3_f32 v65, v65, s19, v161
	v_pk_mul_f32 v[84:85], v[84:85], v[88:89]
	v_pk_fma_f32 v[66:67], v[66:67], s[24:25], v[144:145] op_sel_hi:[1,0,1]
	v_pk_mul_f32 v[80:81], v[80:81], v[84:85]
	v_med3_f32 v66, v66, s19, v161
	v_cvt_pk_fp8_f32 v98, v80, v81
	v_pk_mul_f32 v[80:81], v[76:77], s[30:31] op_sel_hi:[1,0]
	v_med3_f32 v67, v67, s19, v161
	v_exp_f32_e32 v80, v80
	v_exp_f32_e32 v81, v81
	v_pk_fma_f32 v[60:61], v[60:61], s[48:49], v[40:41] op_sel_hi:[1,0,1]
	v_pk_fma_f32 v[56:57], v[56:57], s[24:25], v[140:141] op_sel_hi:[1,0,1]
	v_min_f32_e32 v60, 0x40e00000, v60
	v_pk_add_f32 v[80:81], v[80:81], 1.0 op_sel_hi:[1,0]
	v_min_f32_e32 v61, 0x40e00000, v61
	v_rcp_f32_e32 v80, v80
	v_rcp_f32_e32 v81, v81
	v_med3_f32 v56, v56, s19, v161
	v_med3_f32 v57, v57, s19, v161
	v_pk_fma_f32 v[48:49], v[48:49], s[48:49], v[52:53] op_sel_hi:[1,0,1]
	v_pk_mul_f32 v[76:77], v[76:77], v[80:81]
	v_min_f32_e32 v48, 0x40e00000, v48
	v_pk_mul_f32 v[72:73], v[72:73], v[76:77]
	v_min_f32_e32 v76, 0x40e00000, v78
	v_min_f32_e32 v77, 0x40e00000, v79
	v_pk_mul_f32 v[78:79], v[76:77], s[30:31] op_sel_hi:[1,0]
	v_cvt_pk_fp8_f32 v99, v72, v73
	v_exp_f32_e32 v78, v78
	v_exp_f32_e32 v79, v79
	v_min_f32_e32 v49, 0x40e00000, v49
	v_pk_fma_f32 v[44:45], v[44:45], s[24:25], v[146:147] op_sel_hi:[1,0,1]
	v_pk_fma_f32 v[36:37], v[36:37], s[48:49], v[40:41] op_sel_hi:[1,0,1]
	v_pk_add_f32 v[78:79], v[78:79], 1.0 op_sel_hi:[1,0]
	v_med3_f32 v44, v44, s19, v161
	v_rcp_f32_e32 v78, v78
	v_rcp_f32_e32 v79, v79
	v_med3_f32 v45, v45, s19, v161
	v_min_f32_e32 v36, 0x40e00000, v36
	v_min_f32_e32 v37, 0x40e00000, v37
	v_pk_mul_f32 v[76:77], v[76:77], v[78:79]
	v_pk_fma_f32 v[94:95], v[94:95], s[48:49], v[42:43] op_sel_hi:[1,0,1]
	v_pk_mul_f32 v[74:75], v[74:75], v[76:77]
	v_pk_fma_f32 v[86:87], v[86:87], s[48:49], v[54:55] op_sel_hi:[1,0,1]
	v_cvt_pk_fp8_f32 v99, v74, v75 op_sel:[0,0,1]
	v_pk_mul_f32 v[74:75], v[68:69], s[30:31] op_sel_hi:[1,0]
	v_min_f32_e32 v92, 0x40e00000, v94
	v_exp_f32_e32 v74, v74
	v_exp_f32_e32 v75, v75
	v_min_f32_e32 v93, 0x40e00000, v95
	v_min_f32_e32 v84, 0x40e00000, v86
	v_min_f32_e32 v85, 0x40e00000, v87
	v_pk_add_f32 v[74:75], v[74:75], 1.0 op_sel_hi:[1,0]
	v_pk_mul_f32 v[94:95], v[92:93], s[30:31] op_sel_hi:[1,0]
	v_rcp_f32_e32 v74, v74
	v_rcp_f32_e32 v75, v75
	v_pk_mul_f32 v[86:87], v[84:85], s[30:31] op_sel_hi:[1,0]
	v_exp_f32_e32 v94, v94
	v_exp_f32_e32 v95, v95
	v_pk_mul_f32 v[68:69], v[68:69], v[74:75]
	v_exp_f32_e32 v86, v86
	v_pk_mul_f32 v[68:69], v[64:65], v[68:69]
	v_min_f32_e32 v64, 0x40e00000, v70
	v_min_f32_e32 v65, 0x40e00000, v71
	v_pk_mul_f32 v[70:71], v[64:65], s[30:31] op_sel_hi:[1,0]
	v_exp_f32_e32 v87, v87
	v_exp_f32_e32 v70, v70
	v_exp_f32_e32 v71, v71
	v_pk_fma_f32 v[32:33], v[32:33], s[24:25], v[140:141] op_sel_hi:[1,0,1]
	v_pk_fma_f32 v[62:63], v[62:63], s[48:49], v[42:43] op_sel_hi:[1,0,1]
	v_pk_fma_f32 v[50:51], v[50:51], s[48:49], v[54:55] op_sel_hi:[1,0,1]
	v_pk_add_f32 v[70:71], v[70:71], 1.0 op_sel_hi:[1,0]
	v_pk_fma_f32 v[38:39], v[38:39], s[48:49], v[42:43] op_sel_hi:[1,0,1]
	v_rcp_f32_e32 v70, v70
	v_rcp_f32_e32 v71, v71
	v_med3_f32 v32, v32, s19, v161
	v_med3_f32 v33, v33, s19, v161
	v_pk_add_f32 v[94:95], v[94:95], 1.0 op_sel_hi:[1,0]
	v_pk_mul_f32 v[64:65], v[64:65], v[70:71]
	v_pk_add_f32 v[86:87], v[86:87], 1.0 op_sel_hi:[1,0]
	v_pk_mul_f32 v[66:67], v[66:67], v[64:65]
	v_cvt_pk_fp8_f32 v64, v68, v69
	v_rcp_f32_e32 v94, v94
	v_rcp_f32_e32 v95, v95
	v_cvt_pk_fp8_f32 v64, v66, v67 op_sel:[0,0,1]
	v_pk_mul_f32 v[66:67], v[60:61], s[30:31] op_sel_hi:[1,0]
	v_rcp_f32_e32 v86, v86
	v_exp_f32_e32 v66, v66
	v_exp_f32_e32 v67, v67
	v_rcp_f32_e32 v87, v87
	v_or_b32_e32 v72, 32, v138
	v_pk_fma_f32 v[90:91], v[90:91], s[24:25], v[142:143] op_sel_hi:[1,0,1]
	v_pk_add_f32 v[66:67], v[66:67], 1.0 op_sel_hi:[1,0]
	v_pk_fma_f32 v[82:83], v[82:83], s[24:25], v[144:145] op_sel_hi:[1,0,1]
	v_rcp_f32_e32 v66, v66
	v_rcp_f32_e32 v67, v67
	v_ashrrev_i32_e32 v73, 31, v72
	v_med3_f32 v90, v90, s19, v161
	v_med3_f32 v91, v91, s19, v161
	v_pk_mul_f32 v[60:61], v[60:61], v[66:67]
	s_nop 0
	v_pk_mul_f32 v[56:57], v[56:57], v[60:61]
	v_min_f32_e32 v60, 0x40e00000, v62
	v_cvt_pk_fp8_f32 v65, v56, v57
	v_pk_mul_f32 v[56:57], v[48:49], s[30:31] op_sel_hi:[1,0]
	v_min_f32_e32 v61, 0x40e00000, v63
	v_exp_f32_e32 v56, v56
	v_exp_f32_e32 v57, v57
	v_pk_mul_f32 v[62:63], v[60:61], s[30:31] op_sel_hi:[1,0]
	v_pk_mul_f32 v[92:93], v[92:93], v[94:95]
	v_exp_f32_e32 v62, v62
	v_pk_add_f32 v[56:57], v[56:57], 1.0 op_sel_hi:[1,0]
	v_exp_f32_e32 v63, v63
	v_rcp_f32_e32 v56, v56
	v_rcp_f32_e32 v57, v57
	v_med3_f32 v82, v82, s19, v161
	v_med3_f32 v83, v83, s19, v161
	v_pk_mul_f32 v[84:85], v[84:85], v[86:87]
	v_pk_mul_f32 v[48:49], v[48:49], v[56:57]
	v_lshlrev_b64 v[72:73], 10, v[72:73]
	v_pk_mul_f32 v[44:45], v[44:45], v[48:49]
	v_min_f32_e32 v48, 0x40e00000, v50
	v_cvt_pk_fp8_f32 v66, v44, v45
	v_pk_mul_f32 v[44:45], v[36:37], s[30:31] op_sel_hi:[1,0]
	v_min_f32_e32 v49, 0x40e00000, v51
	v_exp_f32_e32 v44, v44
	v_exp_f32_e32 v45, v45
	v_pk_mul_f32 v[50:51], v[48:49], s[30:31] op_sel_hi:[1,0]
	v_pk_add_f32 v[62:63], v[62:63], 1.0 op_sel_hi:[1,0]
	v_exp_f32_e32 v50, v50
	v_pk_add_f32 v[44:45], v[44:45], 1.0 op_sel_hi:[1,0]
	v_exp_f32_e32 v51, v51
	v_rcp_f32_e32 v44, v44
	v_rcp_f32_e32 v45, v45
	v_pk_mul_f32 v[90:91], v[90:91], v[92:93]
	v_pk_add_f32 v[50:51], v[50:51], 1.0 op_sel_hi:[1,0]
	v_pk_mul_f32 v[82:83], v[82:83], v[84:85]
	v_pk_mul_f32 v[36:37], v[36:37], v[44:45]
	v_lshl_add_u64 v[72:73], s[16:17], 0, v[72:73]
	v_pk_mul_f32 v[32:33], v[32:33], v[36:37]
	v_min_f32_e32 v36, 0x40e00000, v38
	v_min_f32_e32 v37, 0x40e00000, v39
	v_pk_mul_f32 v[38:39], v[36:37], s[30:31] op_sel_hi:[1,0]
	v_rcp_f32_e32 v62, v62
	v_exp_f32_e32 v38, v38
	v_exp_f32_e32 v39, v39
	v_rcp_f32_e32 v63, v63
	v_rcp_f32_e32 v50, v50
	v_rcp_f32_e32 v51, v51
	v_pk_add_f32 v[38:39], v[38:39], 1.0 op_sel_hi:[1,0]
	v_cvt_pk_fp8_f32 v97, v90, v91 op_sel:[0,0,1]
	v_rcp_f32_e32 v38, v38
	v_rcp_f32_e32 v39, v39
	v_cvt_pk_fp8_f32 v98, v82, v83 op_sel:[0,0,1]
	v_lshl_add_u64 v[72:73], v[72:73], 0, v[136:137]
	s_nop 0
	s_nop 1
	v_permlane16_swap_b32 v96, v98
	s_nop 1
	v_permlane16_swap_b32 v97, v99
	global_store_dwordx4 v[72:73], v[96:99], off
	v_add_u32_e32 v72, 0x80, v138
	v_cvt_pk_fp8_f32 v67, v32, v33
	v_pk_fma_f32 v[58:59], v[58:59], s[24:25], v[142:143] op_sel_hi:[1,0,1]
	v_pk_fma_f32 v[46:47], v[46:47], s[24:25], v[144:145] op_sel_hi:[1,0,1]
	v_pk_fma_f32 v[34:35], v[34:35], s[24:25], v[142:143] op_sel_hi:[1,0,1]
	v_ashrrev_i32_e32 v73, 31, v72
	v_med3_f32 v58, v58, s19, v161
	v_med3_f32 v59, v59, s19, v161
	v_pk_mul_f32 v[60:61], v[60:61], v[62:63]
	v_med3_f32 v46, v46, s19, v161
	v_med3_f32 v47, v47, s19, v161
	v_pk_mul_f32 v[48:49], v[48:49], v[50:51]
	v_med3_f32 v34, v34, s19, v161
	v_med3_f32 v35, v35, s19, v161
	v_pk_mul_f32 v[36:37], v[36:37], v[38:39]
	v_lshlrev_b64 v[32:33], 10, v[72:73]
	v_pk_mul_f32 v[58:59], v[58:59], v[60:61]
	v_pk_mul_f32 v[46:47], v[46:47], v[48:49]
	v_pk_mul_f32 v[34:35], v[34:35], v[36:37]
	v_lshl_add_u64 v[32:33], s[16:17], 0, v[32:33]
	v_pk_fma_f32 v[28:29], v[28:29], s[48:49], v[52:53] op_sel_hi:[1,0,1]
	v_cvt_pk_fp8_f32 v65, v58, v59 op_sel:[0,0,1]
	v_cvt_pk_fp8_f32 v66, v46, v47 op_sel:[0,0,1]
	v_cvt_pk_fp8_f32 v67, v34, v35 op_sel:[0,0,1]
	v_lshl_add_u64 v[32:33], v[32:33], 0, v[136:137]
	v_min_f32_e32 v28, 0x40e00000, v28
	v_min_f32_e32 v29, 0x40e00000, v29
	s_nop 1
	v_permlane16_swap_b32 v64, v66
	s_nop 1
	v_permlane16_swap_b32 v65, v67
	global_store_dwordx4 v[32:33], v[64:67], off
	v_pk_mul_f32 v[32:33], v[28:29], s[30:31] op_sel_hi:[1,0]
	v_pk_fma_f32 v[24:25], v[24:25], s[24:25], v[146:147] op_sel_hi:[1,0,1]
	v_exp_f32_e32 v32, v32
	v_exp_f32_e32 v33, v33
	v_pk_fma_f32 v[30:31], v[30:31], s[48:49], v[54:55] op_sel_hi:[1,0,1]
	v_med3_f32 v24, v24, s19, v161
	v_med3_f32 v25, v25, s19, v161
	v_pk_add_f32 v[32:33], v[32:33], 1.0 op_sel_hi:[1,0]
	v_pk_fma_f32 v[26:27], v[26:27], s[24:25], v[144:145] op_sel_hi:[1,0,1]
	v_rcp_f32_e32 v32, v32
	v_rcp_f32_e32 v33, v33
	v_med3_f32 v26, v26, s19, v161
	v_med3_f32 v27, v27, s19, v161
	v_pk_fma_f32 v[20:21], v[20:21], s[48:49], v[40:41] op_sel_hi:[1,0,1]
	v_pk_mul_f32 v[28:29], v[28:29], v[32:33]
	v_min_f32_e32 v20, 0x40e00000, v20
	v_pk_mul_f32 v[28:29], v[24:25], v[28:29]
	v_min_f32_e32 v24, 0x40e00000, v30
	v_min_f32_e32 v25, 0x40e00000, v31
	v_pk_mul_f32 v[30:31], v[24:25], s[30:31] op_sel_hi:[1,0]
	v_min_f32_e32 v21, 0x40e00000, v21
	v_exp_f32_e32 v30, v30
	v_exp_f32_e32 v31, v31
	v_pk_fma_f32 v[16:17], v[16:17], s[24:25], v[140:141] op_sel_hi:[1,0,1]
	v_pk_fma_f32 v[12:13], v[12:13], s[48:49], v[52:53] op_sel_hi:[1,0,1]
	v_med3_f32 v16, v16, s19, v161
	v_pk_add_f32 v[30:31], v[30:31], 1.0 op_sel_hi:[1,0]
	v_med3_f32 v17, v17, s19, v161
	v_rcp_f32_e32 v30, v30
	v_rcp_f32_e32 v31, v31
	v_min_f32_e32 v12, 0x40e00000, v12
	v_min_f32_e32 v13, 0x40e00000, v13
	v_pk_fma_f32 v[8:9], v[8:9], s[24:25], v[146:147] op_sel_hi:[1,0,1]
	v_pk_mul_f32 v[24:25], v[24:25], v[30:31]
	v_med3_f32 v8, v8, s19, v161
	v_pk_mul_f32 v[26:27], v[26:27], v[24:25]
	v_cvt_pk_fp8_f32 v24, v28, v29
	v_med3_f32 v9, v9, s19, v161
	v_pk_fma_f32 v[4:5], v[4:5], s[48:49], v[40:41] op_sel_hi:[1,0,1]
	v_cvt_pk_fp8_f32 v24, v26, v27 op_sel:[0,0,1]
	v_pk_mul_f32 v[26:27], v[20:21], s[30:31] op_sel_hi:[1,0]
	v_min_f32_e32 v4, 0x40e00000, v4
	v_exp_f32_e32 v26, v26
	v_exp_f32_e32 v27, v27
	v_min_f32_e32 v5, 0x40e00000, v5
	v_pk_fma_f32 v[0:1], v[0:1], s[24:25], v[140:141] op_sel_hi:[1,0,1]
	v_pk_fma_f32 v[22:23], v[22:23], s[48:49], v[42:43] op_sel_hi:[1,0,1]
	v_pk_add_f32 v[26:27], v[26:27], 1.0 op_sel_hi:[1,0]
	v_pk_fma_f32 v[14:15], v[14:15], s[48:49], v[54:55] op_sel_hi:[1,0,1]
	v_rcp_f32_e32 v26, v26
	v_rcp_f32_e32 v27, v27
	v_pk_fma_f32 v[6:7], v[6:7], s[48:49], v[42:43] op_sel_hi:[1,0,1]
	v_med3_f32 v0, v0, s19, v161
	v_med3_f32 v1, v1, s19, v161
	v_pk_mul_f32 v[20:21], v[20:21], v[26:27]
	s_nop 0
	v_pk_mul_f32 v[16:17], v[16:17], v[20:21]
	v_min_f32_e32 v20, 0x40e00000, v22
	v_cvt_pk_fp8_f32 v25, v16, v17
	v_pk_mul_f32 v[16:17], v[12:13], s[30:31] op_sel_hi:[1,0]
	v_min_f32_e32 v21, 0x40e00000, v23
	v_exp_f32_e32 v16, v16
	v_exp_f32_e32 v17, v17
	v_pk_mul_f32 v[22:23], v[20:21], s[30:31] op_sel_hi:[1,0]
	s_nop 0
	v_exp_f32_e32 v22, v22
	v_pk_add_f32 v[16:17], v[16:17], 1.0 op_sel_hi:[1,0]
	v_exp_f32_e32 v23, v23
	v_rcp_f32_e32 v16, v16
	v_rcp_f32_e32 v17, v17
	v_pk_fma_f32 v[18:19], v[18:19], s[24:25], v[142:143] op_sel_hi:[1,0,1]
	v_pk_add_f32 v[22:23], v[22:23], 1.0 op_sel_hi:[1,0]
	v_pk_fma_f32 v[10:11], v[10:11], s[24:25], v[144:145] op_sel_hi:[1,0,1]
	v_pk_mul_f32 v[12:13], v[12:13], v[16:17]
	v_rcp_f32_e32 v22, v22
	v_pk_mul_f32 v[8:9], v[8:9], v[12:13]
	v_min_f32_e32 v12, 0x40e00000, v14
	v_cvt_pk_fp8_f32 v26, v8, v9
	v_pk_mul_f32 v[8:9], v[4:5], s[30:31] op_sel_hi:[1,0]
	v_min_f32_e32 v13, 0x40e00000, v15
	v_exp_f32_e32 v8, v8
	v_exp_f32_e32 v9, v9
	v_pk_mul_f32 v[14:15], v[12:13], s[30:31] op_sel_hi:[1,0]
	v_rcp_f32_e32 v23, v23
	v_exp_f32_e32 v14, v14
	v_pk_add_f32 v[8:9], v[8:9], 1.0 op_sel_hi:[1,0]
	v_exp_f32_e32 v15, v15
	v_rcp_f32_e32 v8, v8
	v_rcp_f32_e32 v9, v9
	v_pk_fma_f32 v[2:3], v[2:3], s[24:25], v[142:143] op_sel_hi:[1,0,1]
	v_pk_add_f32 v[14:15], v[14:15], 1.0 op_sel_hi:[1,0]
	v_med3_f32 v18, v18, s19, v161
	v_pk_mul_f32 v[4:5], v[4:5], v[8:9]
	v_rcp_f32_e32 v14, v14
	v_pk_mul_f32 v[0:1], v[0:1], v[4:5]
	v_min_f32_e32 v4, 0x40e00000, v6
	v_min_f32_e32 v5, 0x40e00000, v7
	v_pk_mul_f32 v[6:7], v[4:5], s[30:31] op_sel_hi:[1,0]
	v_rcp_f32_e32 v15, v15
	v_exp_f32_e32 v6, v6
	v_exp_f32_e32 v7, v7
	v_cvt_pk_fp8_f32 v27, v0, v1
	v_add_u32_e32 v0, 0xa0, v138
	v_ashrrev_i32_e32 v1, 31, v0
	v_pk_add_f32 v[6:7], v[6:7], 1.0 op_sel_hi:[1,0]
	v_med3_f32 v19, v19, s19, v161
	v_rcp_f32_e32 v6, v6
	v_rcp_f32_e32 v7, v7
	v_pk_mul_f32 v[20:21], v[20:21], v[22:23]
	v_med3_f32 v10, v10, s19, v161
	v_med3_f32 v11, v11, s19, v161
	v_pk_mul_f32 v[12:13], v[12:13], v[14:15]
	v_med3_f32 v2, v2, s19, v161
	v_med3_f32 v3, v3, s19, v161
	v_pk_mul_f32 v[4:5], v[4:5], v[6:7]
	v_lshlrev_b64 v[0:1], 10, v[0:1]
	v_pk_mul_f32 v[18:19], v[18:19], v[20:21]
	v_pk_mul_f32 v[10:11], v[10:11], v[12:13]
	v_pk_mul_f32 v[2:3], v[2:3], v[4:5]
	v_lshl_add_u64 v[0:1], s[16:17], 0, v[0:1]
	v_cvt_pk_fp8_f32 v25, v18, v19 op_sel:[0,0,1]
	v_cvt_pk_fp8_f32 v26, v10, v11 op_sel:[0,0,1]
	v_cvt_pk_fp8_f32 v27, v2, v3 op_sel:[0,0,1]
	v_lshl_add_u64 v[0:1], v[0:1], 0, v[136:137]
	s_mov_b64 s[24:25], -1
	s_and_b64 vcc, exec, s[2:3]
	s_nop 1
	v_permlane16_swap_b32 v24, v26
	s_nop 1
	v_permlane16_swap_b32 v25, v27
	global_store_dwordx4 v[0:1], v[24:27], off
	s_cbranch_vccnz .LBB0_1031
	v_mov_b32_e32 v0, v185
	v_mov_b32_e32 v1, v185
	s_andn2_b64 vcc, exec, s[8:9]
	s_waitcnt vmcnt(4)
	s_cbranch_vccnz .LBB0_1044
	v_max_i32_e32 v1, 0, v156
	v_max_i32_e32 v2, 0, v157
	v_lshrrev_b32_e32 v1, 2, v1
	v_lshlrev_b32_e32 v2, 14, v2
	v_and_or_b32 v1, v2, s45, v1
	v_mbcnt_lo_u32_b32 v2, -1, 0
	v_mbcnt_hi_u32_b32 v2, -1, v2
	s_mov_b32 s2, s61
	v_lshlrev_b32_e32 v2, 3, v2
	v_readfirstlane_b32 s18, v155
	v_lshl_or_b32 v2, s2, 9, v2
	v_add_u32_e32 v2, s74, v2
	ds_write_b32 v2, v1
	v_max_i32_e32 v1, 0, v158
	v_max_i32_e32 v2, 0, v159
	v_lshrrev_b32_e32 v1, 2, v1
	v_lshlrev_b32_e32 v2, 14, v2
	v_and_or_b32 v1, v2, s45, v1
	v_mbcnt_lo_u32_b32 v2, -1, 0
	v_mbcnt_hi_u32_b32 v2, -1, v2
	s_mov_b32 s2, s61
	v_lshlrev_b32_e32 v2, 3, v2
	s_nop 0
	v_lshl_or_b32 v2, s2, 9, v2
	v_add_u32_e32 v2, s74, v2
	ds_write_b32 v2, v1 offset:4

.LBB0_1128:
	s_lshl_b32 s7, s7, 2
	s_add_i32 s7, s30, s7
	s_add_i32 m0, s7, 0x400
	s_mov_b32 s7, s61
	global_load_lds_dword v[128:129], off
	v_mbcnt_lo_u32_b32 v145, -1, 0
	v_mbcnt_hi_u32_b32 v145, -1, v145
	s_bitcmp1_b32 s79, 0
	v_lshl_or_b32 v128, s7, 6, v145
	s_cselect_b32 s24, 0xc00, 0
	v_readfirstlane_b32 s7, v128
	s_lshr_b32 s29, s7, 1
	s_add_i32 s24, s24, 0
	s_lshl_b32 s26, s26, 8
	s_and_b32 s29, s29, 0x60
	v_lshrrev_b32_e32 v128, 1, v145
	s_add_i32 s24, s24, 0x21000
	v_and_or_b32 v144, v128, 16, s26
	s_lshl_b32 s26, s29, 2
	v_and_b32_e32 v153, 3, v145
	s_and_b32 s7, s7, 0xffffff00
	v_lshlrev_b32_e32 v154, 3, v145
	s_add_i32 s26, s24, s26
	v_lshlrev_b32_e32 v128, 1, v145
	s_add_i32 s24, s24, s7
	v_lshlrev_b32_e32 v153, 2, v153
	v_and_b32_e32 v154, 0x60, v154
	v_and_b32_e32 v128, 0x60, v128
	v_add3_u32 v153, s24, v153, v154
	v_mov_b32_e32 v152, 0x43e00000
	v_add_u32_e32 v128, s26, v128
	v_add_u32_e32 v158, 0x800, v153
	ds_read_b128 v[140:143], v128
	ds_read_b128 v[136:139], v128 offset:16
	ds_read_b128 v[132:135], v128 offset:512
	ds_read_b128 v[128:131], v128 offset:528
	ds_read2_b32 v[154:155], v158 offset1:4
	s_mov_b32 s24, 0x3b800000
	s_waitcnt lgkmcnt(0)
	v_pk_fma_f32 v[124:125], v[124:125], s[24:25], v[140:141] op_sel_hi:[1,0,1]
	v_pk_fma_f32 v[126:127], v[126:127], s[24:25], v[142:143] op_sel_hi:[1,0,1]
	v_pk_fma_f32 v[120:121], v[120:121], s[24:25], v[136:137] op_sel_hi:[1,0,1]
	v_mul_f32_e32 v154, 0x42000000, v154
	v_pk_mul_f32 v[124:125], v[124:125], v[154:155] op_sel_hi:[1,0]
	v_pk_mul_f32 v[126:127], v[126:127], v[154:155] op_sel_hi:[1,0]
	v_pk_mul_f32 v[156:157], v[120:121], v[154:155] op_sel_hi:[1,0]
	v_med3_f32 v121, v124, -v152, v152
	v_med3_f32 v124, v125, -v152, v152
	v_med3_f32 v125, v126, -v152, v152
	v_med3_f32 v126, v127, -v152, v152
	v_cvt_pk_fp8_f32 v120, v121, v124
	v_med3_f32 v124, v156, -v152, v152
	v_med3_f32 v127, v157, -v152, v152
	s_nop 0
	v_cvt_pk_fp8_f32 v121, v124, v127
	v_pk_fma_f32 v[122:123], v[122:123], s[24:25], v[138:139] op_sel_hi:[1,0,1]
	v_pk_fma_f32 v[116:117], v[116:117], s[24:25], v[132:133] op_sel_hi:[1,0,1]
	v_pk_mul_f32 v[122:123], v[122:123], v[154:155] op_sel_hi:[1,0]
	v_pk_fma_f32 v[118:119], v[118:119], s[24:25], v[134:135] op_sel_hi:[1,0,1]
	v_med3_f32 v122, v122, -v152, v152
	v_med3_f32 v123, v123, -v152, v152
	v_pk_mul_f32 v[116:117], v[116:117], v[154:155] op_sel_hi:[1,0]
	v_pk_fma_f32 v[112:113], v[112:113], s[24:25], v[128:129] op_sel_hi:[1,0,1]
	v_cvt_pk_fp8_f32 v121, v122, v123 op_sel:[0,0,1]
	v_pk_mul_f32 v[118:119], v[118:119], v[154:155] op_sel_hi:[1,0]
	v_pk_mul_f32 v[122:123], v[112:113], v[154:155] op_sel_hi:[1,0]
	v_med3_f32 v113, v116, -v152, v152
	v_med3_f32 v116, v117, -v152, v152
	v_med3_f32 v117, v118, -v152, v152
	v_med3_f32 v118, v119, -v152, v152
	v_cvt_pk_fp8_f32 v112, v113, v116
	v_med3_f32 v116, v122, -v152, v152
	v_med3_f32 v119, v123, -v152, v152
	s_nop 0
	v_cvt_pk_fp8_f32 v113, v116, v119
	v_pk_fma_f32 v[114:115], v[114:115], s[24:25], v[130:131] op_sel_hi:[1,0,1]
	v_pk_fma_f32 v[96:97], v[96:97], s[24:25], v[128:129] op_sel_hi:[1,0,1]
	v_pk_mul_f32 v[114:115], v[114:115], v[154:155] op_sel_hi:[1,0]
	v_and_b32_e32 v145, 16, v145
	v_med3_f32 v114, v114, -v152, v152
	v_med3_f32 v115, v115, -v152, v152
	v_cvt_pk_fp8_f32 v113, v114, v115 op_sel:[0,0,1]
	v_mul_f32_e32 v114, 0x42000000, v155
	v_pk_fma_f32 v[110:111], v[110:111], s[24:25], v[142:143] op_sel_hi:[1,0,1]
	v_pk_fma_f32 v[108:109], v[108:109], s[24:25], v[140:141] op_sel_hi:[1,0,1]
	v_pk_fma_f32 v[106:107], v[106:107], s[24:25], v[138:139] op_sel_hi:[1,0,1]
	v_pk_fma_f32 v[104:105], v[104:105], s[24:25], v[136:137] op_sel_hi:[1,0,1]
	v_pk_fma_f32 v[102:103], v[102:103], s[24:25], v[134:135] op_sel_hi:[1,0,1]
	v_pk_fma_f32 v[100:101], v[100:101], s[24:25], v[132:133] op_sel_hi:[1,0,1]
	v_pk_fma_f32 v[98:99], v[98:99], s[24:25], v[130:131] op_sel_hi:[1,0,1]
	v_pk_mul_f32 v[96:97], v[96:97], v[114:115] op_sel_hi:[1,0]
	v_add_u32_e32 v153, v153, v145
	v_pk_mul_f32 v[110:111], v[110:111], v[114:115] op_sel_hi:[1,0]
	v_pk_mul_f32 v[108:109], v[108:109], v[114:115] op_sel_hi:[1,0]
	v_pk_mul_f32 v[106:107], v[106:107], v[114:115] op_sel_hi:[1,0]
	v_pk_mul_f32 v[104:105], v[104:105], v[114:115] op_sel_hi:[1,0]
	v_pk_mul_f32 v[102:103], v[102:103], v[114:115] op_sel_hi:[1,0]
	v_pk_mul_f32 v[100:101], v[100:101], v[114:115] op_sel_hi:[1,0]
	v_pk_mul_f32 v[98:99], v[98:99], v[114:115] op_sel_hi:[1,0]
	v_med3_f32 v96, v96, -v152, v152
	v_med3_f32 v97, v97, -v152, v152
	v_med3_f32 v100, v100, -v152, v152
	v_med3_f32 v101, v101, -v152, v152
	s_nop 0
	v_cvt_pk_fp8_f32 v115, v96, v97
	ds_read_b32 v96, v153 offset:1024
	v_cvt_pk_fp8_f32 v114, v100, v101
	v_med3_f32 v102, v102, -v152, v152
	v_med3_f32 v103, v103, -v152, v152
	v_med3_f32 v108, v108, -v152, v152
	v_med3_f32 v109, v109, -v152, v152
	v_med3_f32 v104, v104, -v152, v152
	v_med3_f32 v105, v105, -v152, v152
	v_cvt_pk_fp8_f32 v114, v102, v103 op_sel:[0,0,1]
	s_waitcnt lgkmcnt(0)
	v_cmp_lt_i32_e32 vcc, -1, v96
	v_mov_b32_e32 v102, 0x40000
	v_cvt_pk_fp8_f32 v122, v108, v109
	v_cvt_pk_fp8_f32 v123, v104, v105
	v_med3_f32 v97, v98, -v152, v152
	v_med3_f32 v98, v99, -v152, v152
	v_cndmask_b32_e32 v96, v102, v96, vcc
	v_cvt_pk_fp8_f32 v115, v97, v98 op_sel:[0,0,1]
	v_ashrrev_i32_e32 v97, 31, v96
	v_or_b32_e32 v144, s29, v144
	v_lshlrev_b64 v[96:97], 10, v[96:97]
	v_ashrrev_i32_e32 v145, 31, v144
	v_med3_f32 v110, v110, -v152, v152
	v_med3_f32 v111, v111, -v152, v152
	v_med3_f32 v104, v106, -v152, v152
	v_med3_f32 v105, v107, -v152, v152
	v_lshl_add_u64 v[96:97], s[12:13], 0, v[96:97]
	v_cvt_pk_fp8_f32 v120, v125, v126 op_sel:[0,0,1]
	v_cvt_pk_fp8_f32 v112, v117, v118 op_sel:[0,0,1]
	v_cvt_pk_fp8_f32 v122, v110, v111 op_sel:[0,0,1]
	v_cvt_pk_fp8_f32 v123, v104, v105 op_sel:[0,0,1]
	v_lshl_add_u64 v[96:97], v[96:97], 0, v[144:145]
	s_nop 1
	v_permlane16_swap_b32 v120, v122
	s_nop 1
	v_permlane16_swap_b32 v121, v123
	global_store_dwordx4 v[96:97], v[120:123], off
	s_nop 1
	v_permlane16_swap_b32 v112, v114
	s_nop 1
	v_permlane16_swap_b32 v113, v115
	ds_read2_b32 v[98:99], v158 offset0:32 offset1:36
	global_store_dwordx4 v[96:97], v[112:115], off offset:128
	v_pk_fma_f32 v[92:93], v[92:93], s[24:25], v[140:141] op_sel_hi:[1,0,1]
	v_pk_fma_f32 v[94:95], v[94:95], s[24:25], v[142:143] op_sel_hi:[1,0,1]
	v_pk_fma_f32 v[88:89], v[88:89], s[24:25], v[136:137] op_sel_hi:[1,0,1]
	s_waitcnt lgkmcnt(0)
	v_mul_f32_e32 v96, 0x42000000, v98
	v_pk_mul_f32 v[92:93], v[92:93], v[96:97] op_sel_hi:[1,0]
	v_pk_mul_f32 v[94:95], v[94:95], v[96:97] op_sel_hi:[1,0]
	v_pk_mul_f32 v[100:101], v[88:89], v[96:97] op_sel_hi:[1,0]
	v_med3_f32 v89, v92, -v152, v152
	v_med3_f32 v92, v93, -v152, v152
	v_med3_f32 v93, v94, -v152, v152
	v_med3_f32 v94, v95, -v152, v152
	v_cvt_pk_fp8_f32 v88, v89, v92
	v_med3_f32 v92, v100, -v152, v152
	v_med3_f32 v95, v101, -v152, v152
	s_nop 0
	v_cvt_pk_fp8_f32 v89, v92, v95
	v_pk_fma_f32 v[90:91], v[90:91], s[24:25], v[138:139] op_sel_hi:[1,0,1]
	v_pk_fma_f32 v[84:85], v[84:85], s[24:25], v[132:133] op_sel_hi:[1,0,1]
	v_pk_mul_f32 v[90:91], v[90:91], v[96:97] op_sel_hi:[1,0]
	v_pk_fma_f32 v[86:87], v[86:87], s[24:25], v[134:135] op_sel_hi:[1,0,1]
	v_med3_f32 v90, v90, -v152, v152
	v_med3_f32 v91, v91, -v152, v152
	v_pk_mul_f32 v[84:85], v[84:85], v[96:97] op_sel_hi:[1,0]
	v_pk_fma_f32 v[80:81], v[80:81], s[24:25], v[128:129] op_sel_hi:[1,0,1]
	v_cvt_pk_fp8_f32 v89, v90, v91 op_sel:[0,0,1]
	v_pk_mul_f32 v[86:87], v[86:87], v[96:97] op_sel_hi:[1,0]
	v_pk_mul_f32 v[90:91], v[80:81], v[96:97] op_sel_hi:[1,0]
	v_med3_f32 v81, v84, -v152, v152
	v_med3_f32 v84, v85, -v152, v152
	v_med3_f32 v85, v86, -v152, v152
	v_med3_f32 v86, v87, -v152, v152
	v_cvt_pk_fp8_f32 v80, v81, v84
	v_med3_f32 v84, v90, -v152, v152
	v_med3_f32 v87, v91, -v152, v152
	s_nop 0
	v_cvt_pk_fp8_f32 v81, v84, v87
	v_pk_fma_f32 v[82:83], v[82:83], s[24:25], v[130:131] op_sel_hi:[1,0,1]
	v_pk_fma_f32 v[64:65], v[64:65], s[24:25], v[128:129] op_sel_hi:[1,0,1]
	v_pk_mul_f32 v[82:83], v[82:83], v[96:97] op_sel_hi:[1,0]
	v_pk_fma_f32 v[78:79], v[78:79], s[24:25], v[142:143] op_sel_hi:[1,0,1]
	v_med3_f32 v82, v82, -v152, v152
	v_med3_f32 v83, v83, -v152, v152
	v_cvt_pk_fp8_f32 v81, v82, v83 op_sel:[0,0,1]
	v_mul_f32_e32 v82, 0x42000000, v99
	v_pk_fma_f32 v[76:77], v[76:77], s[24:25], v[140:141] op_sel_hi:[1,0,1]
	v_pk_fma_f32 v[74:75], v[74:75], s[24:25], v[138:139] op_sel_hi:[1,0,1]
	v_pk_fma_f32 v[72:73], v[72:73], s[24:25], v[136:137] op_sel_hi:[1,0,1]
	v_pk_fma_f32 v[70:71], v[70:71], s[24:25], v[134:135] op_sel_hi:[1,0,1]
	v_pk_fma_f32 v[68:69], v[68:69], s[24:25], v[132:133] op_sel_hi:[1,0,1]
	v_pk_fma_f32 v[66:67], v[66:67], s[24:25], v[130:131] op_sel_hi:[1,0,1]
	v_pk_mul_f32 v[64:65], v[64:65], v[82:83] op_sel_hi:[1,0]
	v_pk_mul_f32 v[78:79], v[78:79], v[82:83] op_sel_hi:[1,0]
	v_pk_mul_f32 v[76:77], v[76:77], v[82:83] op_sel_hi:[1,0]
	v_pk_mul_f32 v[74:75], v[74:75], v[82:83] op_sel_hi:[1,0]
	v_pk_mul_f32 v[72:73], v[72:73], v[82:83] op_sel_hi:[1,0]
	v_pk_mul_f32 v[70:71], v[70:71], v[82:83] op_sel_hi:[1,0]
	v_pk_mul_f32 v[68:69], v[68:69], v[82:83] op_sel_hi:[1,0]
	v_pk_mul_f32 v[66:67], v[66:67], v[82:83] op_sel_hi:[1,0]
	v_med3_f32 v64, v64, -v152, v152
	v_med3_f32 v65, v65, -v152, v152
	s_nop 0
	v_cvt_pk_fp8_f32 v83, v64, v65
	ds_read_b32 v64, v153 offset:1152
	v_med3_f32 v76, v76, -v152, v152
	v_med3_f32 v77, v77, -v152, v152
	v_med3_f32 v72, v72, -v152, v152
	v_med3_f32 v73, v73, -v152, v152
	v_med3_f32 v68, v68, -v152, v152
	v_med3_f32 v69, v69, -v152, v152
	s_waitcnt lgkmcnt(0)
	v_cmp_lt_i32_e32 vcc, -1, v64
	v_cvt_pk_fp8_f32 v90, v76, v77
	v_cvt_pk_fp8_f32 v91, v72, v73
	v_cvt_pk_fp8_f32 v82, v68, v69
	v_med3_f32 v65, v66, -v152, v152
	v_med3_f32 v66, v67, -v152, v152
	v_cndmask_b32_e32 v64, v102, v64, vcc
	v_cvt_pk_fp8_f32 v83, v65, v66 op_sel:[0,0,1]
	v_ashrrev_i32_e32 v65, 31, v64
	v_lshlrev_b64 v[64:65], 10, v[64:65]
	v_med3_f32 v78, v78, -v152, v152
	v_med3_f32 v79, v79, -v152, v152
	v_med3_f32 v72, v74, -v152, v152
	v_med3_f32 v73, v75, -v152, v152
	v_med3_f32 v70, v70, -v152, v152
	v_med3_f32 v71, v71, -v152, v152
	v_lshl_add_u64 v[64:65], s[12:13], 0, v[64:65]
	v_cvt_pk_fp8_f32 v88, v93, v94 op_sel:[0,0,1]
	v_cvt_pk_fp8_f32 v80, v85, v86 op_sel:[0,0,1]
	v_cvt_pk_fp8_f32 v90, v78, v79 op_sel:[0,0,1]
	v_cvt_pk_fp8_f32 v91, v72, v73 op_sel:[0,0,1]
	v_cvt_pk_fp8_f32 v82, v70, v71 op_sel:[0,0,1]
	v_lshl_add_u64 v[64:65], v[64:65], 0, v[144:145]
	s_nop 1
	v_permlane16_swap_b32 v88, v90
	s_nop 1
	v_permlane16_swap_b32 v89, v91
	global_store_dwordx4 v[64:65], v[88:91], off
	s_nop 1
	v_permlane16_swap_b32 v80, v82
	s_nop 1
	v_permlane16_swap_b32 v81, v83
	ds_read2_b32 v[66:67], v158 offset0:128 offset1:132
	global_store_dwordx4 v[64:65], v[80:83], off offset:128
	v_pk_fma_f32 v[60:61], v[60:61], s[24:25], v[140:141] op_sel_hi:[1,0,1]
	v_pk_fma_f32 v[62:63], v[62:63], s[24:25], v[142:143] op_sel_hi:[1,0,1]
	v_pk_fma_f32 v[56:57], v[56:57], s[24:25], v[136:137] op_sel_hi:[1,0,1]
	s_waitcnt lgkmcnt(0)
	v_mul_f32_e32 v64, 0x42000000, v66
	v_pk_mul_f32 v[60:61], v[60:61], v[64:65] op_sel_hi:[1,0]
	v_pk_mul_f32 v[62:63], v[62:63], v[64:65] op_sel_hi:[1,0]
	v_pk_mul_f32 v[68:69], v[56:57], v[64:65] op_sel_hi:[1,0]
	v_med3_f32 v57, v60, -v152, v152
	v_med3_f32 v60, v61, -v152, v152
	v_med3_f32 v61, v62, -v152, v152
	v_med3_f32 v62, v63, -v152, v152
	v_cvt_pk_fp8_f32 v56, v57, v60
	v_med3_f32 v60, v68, -v152, v152
	v_med3_f32 v63, v69, -v152, v152
	s_nop 0
	v_cvt_pk_fp8_f32 v57, v60, v63
	v_pk_fma_f32 v[58:59], v[58:59], s[24:25], v[138:139] op_sel_hi:[1,0,1]
	v_pk_fma_f32 v[52:53], v[52:53], s[24:25], v[132:133] op_sel_hi:[1,0,1]
	v_pk_mul_f32 v[58:59], v[58:59], v[64:65] op_sel_hi:[1,0]
	v_pk_fma_f32 v[54:55], v[54:55], s[24:25], v[134:135] op_sel_hi:[1,0,1]
	v_med3_f32 v58, v58, -v152, v152
	v_med3_f32 v59, v59, -v152, v152
	v_pk_mul_f32 v[52:53], v[52:53], v[64:65] op_sel_hi:[1,0]
	v_pk_fma_f32 v[48:49], v[48:49], s[24:25], v[128:129] op_sel_hi:[1,0,1]
	v_cvt_pk_fp8_f32 v57, v58, v59 op_sel:[0,0,1]
	v_pk_mul_f32 v[54:55], v[54:55], v[64:65] op_sel_hi:[1,0]
	v_pk_mul_f32 v[58:59], v[48:49], v[64:65] op_sel_hi:[1,0]
	v_med3_f32 v49, v52, -v152, v152
	v_med3_f32 v52, v53, -v152, v152
	v_med3_f32 v53, v54, -v152, v152
	v_med3_f32 v54, v55, -v152, v152
	v_cvt_pk_fp8_f32 v48, v49, v52
	v_med3_f32 v52, v58, -v152, v152
	v_med3_f32 v55, v59, -v152, v152
	s_nop 0
	v_cvt_pk_fp8_f32 v49, v52, v55
	v_pk_fma_f32 v[50:51], v[50:51], s[24:25], v[130:131] op_sel_hi:[1,0,1]
	v_pk_fma_f32 v[32:33], v[32:33], s[24:25], v[128:129] op_sel_hi:[1,0,1]
	v_pk_mul_f32 v[50:51], v[50:51], v[64:65] op_sel_hi:[1,0]
	v_pk_fma_f32 v[46:47], v[46:47], s[24:25], v[142:143] op_sel_hi:[1,0,1]
	v_med3_f32 v50, v50, -v152, v152
	v_med3_f32 v51, v51, -v152, v152
	v_cvt_pk_fp8_f32 v49, v50, v51 op_sel:[0,0,1]
	v_mul_f32_e32 v50, 0x42000000, v67
	v_pk_fma_f32 v[44:45], v[44:45], s[24:25], v[140:141] op_sel_hi:[1,0,1]
	v_pk_fma_f32 v[42:43], v[42:43], s[24:25], v[138:139] op_sel_hi:[1,0,1]
	v_pk_fma_f32 v[40:41], v[40:41], s[24:25], v[136:137] op_sel_hi:[1,0,1]
	v_pk_fma_f32 v[38:39], v[38:39], s[24:25], v[134:135] op_sel_hi:[1,0,1]
	v_pk_fma_f32 v[36:37], v[36:37], s[24:25], v[132:133] op_sel_hi:[1,0,1]
	v_pk_fma_f32 v[34:35], v[34:35], s[24:25], v[130:131] op_sel_hi:[1,0,1]
	v_pk_mul_f32 v[32:33], v[32:33], v[50:51] op_sel_hi:[1,0]
	v_pk_mul_f32 v[46:47], v[46:47], v[50:51] op_sel_hi:[1,0]
	v_pk_mul_f32 v[44:45], v[44:45], v[50:51] op_sel_hi:[1,0]
	v_pk_mul_f32 v[42:43], v[42:43], v[50:51] op_sel_hi:[1,0]
	v_pk_mul_f32 v[40:41], v[40:41], v[50:51] op_sel_hi:[1,0]
	v_pk_mul_f32 v[38:39], v[38:39], v[50:51] op_sel_hi:[1,0]
	v_pk_mul_f32 v[36:37], v[36:37], v[50:51] op_sel_hi:[1,0]
	v_pk_mul_f32 v[34:35], v[34:35], v[50:51] op_sel_hi:[1,0]
	v_med3_f32 v32, v32, -v152, v152
	v_med3_f32 v33, v33, -v152, v152
	s_nop 0
	v_cvt_pk_fp8_f32 v51, v32, v33
	ds_read_b32 v32, v153 offset:1536
	v_med3_f32 v44, v44, -v152, v152
	v_med3_f32 v45, v45, -v152, v152
	v_med3_f32 v40, v40, -v152, v152
	v_med3_f32 v41, v41, -v152, v152
	v_med3_f32 v36, v36, -v152, v152
	v_med3_f32 v37, v37, -v152, v152
	s_waitcnt lgkmcnt(0)
	v_cmp_lt_i32_e32 vcc, -1, v32
	v_cvt_pk_fp8_f32 v58, v44, v45
	v_cvt_pk_fp8_f32 v59, v40, v41
	v_cvt_pk_fp8_f32 v50, v36, v37
	v_med3_f32 v33, v34, -v152, v152
	v_med3_f32 v34, v35, -v152, v152
	v_cndmask_b32_e32 v32, v102, v32, vcc
	v_cvt_pk_fp8_f32 v51, v33, v34 op_sel:[0,0,1]
	v_ashrrev_i32_e32 v33, 31, v32
	v_lshlrev_b64 v[32:33], 10, v[32:33]
	v_med3_f32 v46, v46, -v152, v152
	v_med3_f32 v47, v47, -v152, v152
	v_med3_f32 v40, v42, -v152, v152
	v_med3_f32 v41, v43, -v152, v152
	v_med3_f32 v38, v38, -v152, v152
	v_med3_f32 v39, v39, -v152, v152
	v_lshl_add_u64 v[32:33], s[12:13], 0, v[32:33]
	v_cvt_pk_fp8_f32 v56, v61, v62 op_sel:[0,0,1]
	v_cvt_pk_fp8_f32 v48, v53, v54 op_sel:[0,0,1]
	v_cvt_pk_fp8_f32 v58, v46, v47 op_sel:[0,0,1]
	v_cvt_pk_fp8_f32 v59, v40, v41 op_sel:[0,0,1]
	v_cvt_pk_fp8_f32 v50, v38, v39 op_sel:[0,0,1]
	v_lshl_add_u64 v[32:33], v[32:33], 0, v[144:145]
	s_nop 1
	v_permlane16_swap_b32 v56, v58
	s_nop 1
	v_permlane16_swap_b32 v57, v59
	global_store_dwordx4 v[32:33], v[56:59], off
	s_nop 1
	v_permlane16_swap_b32 v48, v50
	s_nop 1
	v_permlane16_swap_b32 v49, v51
	ds_read2_b32 v[34:35], v158 offset0:160 offset1:164
	global_store_dwordx4 v[32:33], v[48:51], off offset:128
	v_pk_fma_f32 v[28:29], v[28:29], s[24:25], v[140:141] op_sel_hi:[1,0,1]
	v_pk_fma_f32 v[30:31], v[30:31], s[24:25], v[142:143] op_sel_hi:[1,0,1]
	v_pk_fma_f32 v[24:25], v[24:25], s[24:25], v[136:137] op_sel_hi:[1,0,1]
	s_waitcnt lgkmcnt(0)
	v_mul_f32_e32 v32, 0x42000000, v34
	v_pk_mul_f32 v[28:29], v[28:29], v[32:33] op_sel_hi:[1,0]
	v_pk_mul_f32 v[30:31], v[30:31], v[32:33] op_sel_hi:[1,0]
	v_pk_mul_f32 v[36:37], v[24:25], v[32:33] op_sel_hi:[1,0]
	v_med3_f32 v25, v28, -v152, v152
	v_med3_f32 v28, v29, -v152, v152
	v_med3_f32 v29, v30, -v152, v152
	v_med3_f32 v30, v31, -v152, v152
	v_cvt_pk_fp8_f32 v24, v25, v28
	v_med3_f32 v28, v36, -v152, v152
	v_med3_f32 v31, v37, -v152, v152
	s_nop 0
	v_cvt_pk_fp8_f32 v25, v28, v31
	v_pk_fma_f32 v[26:27], v[26:27], s[24:25], v[138:139] op_sel_hi:[1,0,1]
	v_pk_fma_f32 v[20:21], v[20:21], s[24:25], v[132:133] op_sel_hi:[1,0,1]
	v_pk_mul_f32 v[26:27], v[26:27], v[32:33] op_sel_hi:[1,0]
	v_pk_fma_f32 v[22:23], v[22:23], s[24:25], v[134:135] op_sel_hi:[1,0,1]
	v_med3_f32 v26, v26, -v152, v152
	v_med3_f32 v27, v27, -v152, v152
	v_pk_mul_f32 v[20:21], v[20:21], v[32:33] op_sel_hi:[1,0]
	v_pk_fma_f32 v[16:17], v[16:17], s[24:25], v[128:129] op_sel_hi:[1,0,1]
	v_cvt_pk_fp8_f32 v25, v26, v27 op_sel:[0,0,1]
	v_pk_mul_f32 v[22:23], v[22:23], v[32:33] op_sel_hi:[1,0]
	v_pk_mul_f32 v[26:27], v[16:17], v[32:33] op_sel_hi:[1,0]
	v_med3_f32 v17, v20, -v152, v152
	v_med3_f32 v20, v21, -v152, v152
	v_med3_f32 v21, v22, -v152, v152
	v_med3_f32 v22, v23, -v152, v152
	v_cvt_pk_fp8_f32 v16, v17, v20
	v_med3_f32 v20, v26, -v152, v152
	v_med3_f32 v23, v27, -v152, v152
	s_nop 0
	v_cvt_pk_fp8_f32 v17, v20, v23
	v_pk_fma_f32 v[18:19], v[18:19], s[24:25], v[130:131] op_sel_hi:[1,0,1]
	v_pk_fma_f32 v[0:1], v[0:1], s[24:25], v[128:129] op_sel_hi:[1,0,1]
	v_pk_mul_f32 v[18:19], v[18:19], v[32:33] op_sel_hi:[1,0]
	v_pk_fma_f32 v[14:15], v[14:15], s[24:25], v[142:143] op_sel_hi:[1,0,1]
	v_med3_f32 v18, v18, -v152, v152
	v_med3_f32 v19, v19, -v152, v152
	v_cvt_pk_fp8_f32 v17, v18, v19 op_sel:[0,0,1]
	v_mul_f32_e32 v18, 0x42000000, v35
	v_pk_fma_f32 v[12:13], v[12:13], s[24:25], v[140:141] op_sel_hi:[1,0,1]
	v_pk_fma_f32 v[10:11], v[10:11], s[24:25], v[138:139] op_sel_hi:[1,0,1]
	v_pk_fma_f32 v[8:9], v[8:9], s[24:25], v[136:137] op_sel_hi:[1,0,1]
	v_pk_fma_f32 v[6:7], v[6:7], s[24:25], v[134:135] op_sel_hi:[1,0,1]
	v_pk_fma_f32 v[4:5], v[4:5], s[24:25], v[132:133] op_sel_hi:[1,0,1]
	v_pk_fma_f32 v[2:3], v[2:3], s[24:25], v[130:131] op_sel_hi:[1,0,1]
	v_pk_mul_f32 v[0:1], v[0:1], v[18:19] op_sel_hi:[1,0]
	v_pk_mul_f32 v[14:15], v[14:15], v[18:19] op_sel_hi:[1,0]
	v_pk_mul_f32 v[12:13], v[12:13], v[18:19] op_sel_hi:[1,0]
	v_pk_mul_f32 v[10:11], v[10:11], v[18:19] op_sel_hi:[1,0]
	v_pk_mul_f32 v[8:9], v[8:9], v[18:19] op_sel_hi:[1,0]
	v_pk_mul_f32 v[6:7], v[6:7], v[18:19] op_sel_hi:[1,0]
	v_pk_mul_f32 v[4:5], v[4:5], v[18:19] op_sel_hi:[1,0]
	v_pk_mul_f32 v[2:3], v[2:3], v[18:19] op_sel_hi:[1,0]
	v_med3_f32 v0, v0, -v152, v152
	v_med3_f32 v1, v1, -v152, v152
	s_nop 0
	v_cvt_pk_fp8_f32 v19, v0, v1
	ds_read_b32 v0, v153 offset:1664
	v_med3_f32 v12, v12, -v152, v152
	v_med3_f32 v13, v13, -v152, v152
	v_med3_f32 v8, v8, -v152, v152
	v_med3_f32 v9, v9, -v152, v152
	v_med3_f32 v4, v4, -v152, v152
	v_med3_f32 v5, v5, -v152, v152
	s_waitcnt lgkmcnt(0)
	v_cmp_lt_i32_e32 vcc, -1, v0
	v_cvt_pk_fp8_f32 v26, v12, v13
	v_cvt_pk_fp8_f32 v27, v8, v9
	v_cvt_pk_fp8_f32 v18, v4, v5
	v_med3_f32 v1, v2, -v152, v152
	v_med3_f32 v2, v3, -v152, v152
	v_cndmask_b32_e32 v0, v102, v0, vcc
	v_cvt_pk_fp8_f32 v19, v1, v2 op_sel:[0,0,1]
	v_ashrrev_i32_e32 v1, 31, v0
	v_lshlrev_b64 v[0:1], 10, v[0:1]
	v_med3_f32 v14, v14, -v152, v152
	v_med3_f32 v15, v15, -v152, v152
	v_med3_f32 v8, v10, -v152, v152
	v_med3_f32 v9, v11, -v152, v152
	v_med3_f32 v6, v6, -v152, v152
	v_med3_f32 v7, v7, -v152, v152
	v_lshl_add_u64 v[0:1], s[12:13], 0, v[0:1]
	v_cvt_pk_fp8_f32 v24, v29, v30 op_sel:[0,0,1]
	v_cvt_pk_fp8_f32 v16, v21, v22 op_sel:[0,0,1]
	v_cvt_pk_fp8_f32 v26, v14, v15 op_sel:[0,0,1]
	v_cvt_pk_fp8_f32 v27, v8, v9 op_sel:[0,0,1]
	v_cvt_pk_fp8_f32 v18, v6, v7 op_sel:[0,0,1]
	v_lshl_add_u64 v[0:1], v[0:1], 0, v[144:145]
	s_and_b64 vcc, exec, s[2:3]
	s_mov_b64 s[2:3], -1
	s_nop 1
	v_permlane16_swap_b32 v24, v26
	s_nop 1
	v_permlane16_swap_b32 v25, v27
	global_store_dwordx4 v[0:1], v[24:27], off
	s_nop 1
	v_permlane16_swap_b32 v16, v18
	s_nop 1
	v_permlane16_swap_b32 v17, v19
	global_store_dwordx4 v[0:1], v[16:19], off offset:128
	s_cbranch_vccnz .LBB0_1110
	v_mov_b32_e32 v0, v185
	s_waitcnt vmcnt(8)
	s_andn2_b64 vcc, exec, s[10:11]
	s_cbranch_vccnz .LBB0_1131
	v_mov_b32_e32 v1, s78
	ds_read_b32 v1, v1
	s_waitcnt lgkmcnt(0)
	v_readfirstlane_b32 s6, v1
